# P0 w_down weight transposer: hand-written double-buffered loop (next item loads in flight while current item transposes)
# baseline (speedup 1.0000x reference)
; #define GAS __attribute__((address_space(1)))
; #define LAS __attribute__((address_space(3)))
;     const int pr = item >> 1, kb = 2 * (pr / nblk) + (item & 1), nb = pr % nblk, k0 = 64 * kb, n0 = 32 * nb;
;     const int nr = n0 + (lane & 31); const int sc = MAP == 1 ? src_col_in(nr) : nr;
;     float v[32];
; #pragma unroll
;     for (int i = 0; i < 32; ++i) v[i] = sc >= 0 ? W[(size_t)(k0 + 2 * i + (lane >> 5)) * Nsrc + sc] : 0.f;
; #pragma unroll
;     for (int i = 0; i < 32; ++i) { const int k = k0 + 2 * i + (lane >> 5); float x = v[i] * wscale; if (KS) x *= (k < ksplit ? ksA[k] : ksB[k - ksplit]); scr[(2 * i + (lane >> 5)) * 33 + (lane & 31)] = x; }
;     LDS_WAIT(); asm volatile("" ::: "memory");
;     const int c = lane & 7;
; #pragma unroll
;     for (int j = 0; j < 4; ++j) { const int n = (lane >> 3) + 8 * j; const LAS float* s = scr + (8 * c) * 33 + n;
;         const unsigned long long o = (unsigned long long)pg8::pk4_fp8(s[0 * 33], s[1 * 33], s[2 * 33], s[3 * 33]) | ((unsigned long long)pg8::pk4_fp8(s[4 * 33], s[5 * 33], s[6 * 33], s[7 * 33]) << 32);
;         *(GAS unsigned long long*)(WT + (size_t)(n0 + n) * K + k0 + 8 * c) = o; }
;     LDS_WAIT(); asm volatile("" ::: "memory");
; }
; __global__ void __launch_bounds__(NWAVES * 64, 2) hybrid_fwd(Args args) {
;     ...
;         for (int it = gw; it < DEPTH * I_L; it += NGW) {
;             const int l = it / I_L; int r = it % I_L;
;             if (r < I_IN) { if (l >= PROJ_F8_FROM) p0_transpose_item_f8<true, 1>(args.in[2] + (size_t)l * DM * NSRC, DM, NSRC, NPROJ / 32, (unsigned char*)(ws + WS_WIN + l * SZ_WIN), WUP8_SCALE, args.in[1] + l * DM, args.in[1] + l * DM, DM, scr, r, lane);
;                 else p0_transpose_item<1, true>(args.in[2] + (size_t)l * DM * NSRC, DM, NSRC, NPROJ / 32, (bf16*)(ws + WS_WIN + l * SZ_WIN), args.in[1] + l * DM, args.in[1] + l * DM, DM, scr, r, lane); continue; } r -= I_IN;
;             if (r < I_O) { if (l >= WO_F8_FROM) p0_transpose_item_f8<true>(args.in[13] + (size_t)l * DM * DM, DM, DM, DM / 32, (unsigned char*)(ws + WS_WO + l * SZ_WO), 64.f, args.in[6] + l * 2048, args.in[12] + l * 2048, 2048, scr, r, lane);
;                 else p0_transpose_item<0, true>(args.in[13] + (size_t)l * DM * DM, DM, DM, DM / 32, (bf16*)(ws + WS_WO + l * SZ_WO), args.in[6] + l * 2048, args.in[12] + l * 2048, 2048, scr, r, lane); continue; } r -= I_O;
.LBB0_15:
	s_mul_hi_i32 s0, s50, 0xad602b59
	s_add_i32 s0, s0, s50
	s_lshr_b32 s1, s0, 31
	s_ashr_i32 s0, s0, 16
	s_add_i32 s58, s0, s1
	s_mul_i32 s0, s58, 0xfffe8600
	s_add_i32 s51, s50, s0
	s_cmpk_gt_i32 s51, 0x59ff
	s_mov_b64 s[0:1], -1
	s_cbranch_scc0 .LBB0_28
	s_cmpk_gt_u32 s51, 0x79ff
	s_cbranch_scc0 .LBB0_22
	s_ashr_i32 s59, s58, 31
	s_lshl_b64 s[60:61], s[58:59], 28
	s_lshl_b64 s[0:1], s[58:59], 27
	s_cmpk_gt_u32 s51, 0xf9ff
	s_mov_b64 s[20:21], -1
	s_cbranch_scc0 .LBB0_19
	s_add_i32 s4, s51, s96
	s_cmp_gt_i32 s4, 0x179ff
	s_cbranch_scc1 .Lwd_orig
	v_readlane_b32 s4, v253, 35
	v_readlane_b32 s5, v253, 36
	s_add_u32 s10, s4, s60
	s_addc_u32 s11, s5, s61
	s_add_u32 s30, s81, s0
	s_addc_u32 s31, s94, s1
	s_add_i32 s20, s51, 0xffff0600
	s_lshr_b32 s16, s20, 7
	s_and_b32 s16, s16, 0xfe
	s_and_b32 s36, s20, 1
	s_or_b32 s16, s16, s36
	s_lshl_b32 s16, s16, 6
	s_lshl_b32 s36, s20, 4
	s_and_b32 s36, s36, 0xfe0
	v_or_b32_e32 v208, s16, v6
	v_lshlrev_b32_e32 v208, 12, v208
	v_or3_b32 v208, s36, v18, v208
	v_lshlrev_b32_e32 v208, 2, v208
	s_mov_b64 s[8:9], s[10:11]
	global_load_dword v144, v208, s[8:9]
	s_add_u32 s8, s8, 0x8000
	s_addc_u32 s9, s9, 0
	global_load_dword v145, v208, s[8:9]
	s_add_u32 s8, s8, 0x8000
	s_addc_u32 s9, s9, 0
	global_load_dword v146, v208, s[8:9]
	s_add_u32 s8, s8, 0x8000
	s_addc_u32 s9, s9, 0
	global_load_dword v147, v208, s[8:9]
	s_add_u32 s8, s8, 0x8000
	s_addc_u32 s9, s9, 0
	global_load_dword v148, v208, s[8:9]
	s_add_u32 s8, s8, 0x8000
	s_addc_u32 s9, s9, 0
	global_load_dword v149, v208, s[8:9]
	s_add_u32 s8, s8, 0x8000
	s_addc_u32 s9, s9, 0
	global_load_dword v150, v208, s[8:9]
	s_add_u32 s8, s8, 0x8000
	s_addc_u32 s9, s9, 0
	global_load_dword v151, v208, s[8:9]
	s_add_u32 s8, s8, 0x8000
	s_addc_u32 s9, s9, 0
	global_load_dword v152, v208, s[8:9]
	s_add_u32 s8, s8, 0x8000
	s_addc_u32 s9, s9, 0
	global_load_dword v153, v208, s[8:9]
	s_add_u32 s8, s8, 0x8000
	s_addc_u32 s9, s9, 0
	global_load_dword v154, v208, s[8:9]
	s_add_u32 s8, s8, 0x8000
	s_addc_u32 s9, s9, 0
	global_load_dword v155, v208, s[8:9]
	s_add_u32 s8, s8, 0x8000
	s_addc_u32 s9, s9, 0
	global_load_dword v156, v208, s[8:9]
	s_add_u32 s8, s8, 0x8000
	s_addc_u32 s9, s9, 0
	global_load_dword v157, v208, s[8:9]
	s_add_u32 s8, s8, 0x8000
	s_addc_u32 s9, s9, 0
	global_load_dword v158, v208, s[8:9]
	s_add_u32 s8, s8, 0x8000
	s_addc_u32 s9, s9, 0
	global_load_dword v159, v208, s[8:9]
	s_add_u32 s8, s8, 0x8000
	s_addc_u32 s9, s9, 0
	global_load_dword v160, v208, s[8:9]
	s_add_u32 s8, s8, 0x8000
	s_addc_u32 s9, s9, 0
	global_load_dword v161, v208, s[8:9]
	s_add_u32 s8, s8, 0x8000
	s_addc_u32 s9, s9, 0
	global_load_dword v162, v208, s[8:9]
	s_add_u32 s8, s8, 0x8000
	s_addc_u32 s9, s9, 0
	global_load_dword v163, v208, s[8:9]
	s_add_u32 s8, s8, 0x8000
	s_addc_u32 s9, s9, 0
	global_load_dword v164, v208, s[8:9]
	s_add_u32 s8, s8, 0x8000
	s_addc_u32 s9, s9, 0
	global_load_dword v165, v208, s[8:9]
	s_add_u32 s8, s8, 0x8000
	s_addc_u32 s9, s9, 0
	global_load_dword v166, v208, s[8:9]
	s_add_u32 s8, s8, 0x8000
	s_addc_u32 s9, s9, 0
	global_load_dword v167, v208, s[8:9]
	s_add_u32 s8, s8, 0x8000
	s_addc_u32 s9, s9, 0
	global_load_dword v168, v208, s[8:9]
	s_add_u32 s8, s8, 0x8000
	s_addc_u32 s9, s9, 0
	global_load_dword v169, v208, s[8:9]
	s_add_u32 s8, s8, 0x8000
	s_addc_u32 s9, s9, 0
	global_load_dword v170, v208, s[8:9]
	s_add_u32 s8, s8, 0x8000
	s_addc_u32 s9, s9, 0
	global_load_dword v171, v208, s[8:9]
	s_add_u32 s8, s8, 0x8000
	s_addc_u32 s9, s9, 0
	global_load_dword v172, v208, s[8:9]
	s_add_u32 s8, s8, 0x8000
	s_addc_u32 s9, s9, 0
	global_load_dword v173, v208, s[8:9]
	s_add_u32 s8, s8, 0x8000
	s_addc_u32 s9, s9, 0
	global_load_dword v174, v208, s[8:9]
	s_add_u32 s8, s8, 0x8000
	s_addc_u32 s9, s9, 0
	global_load_dword v175, v208, s[8:9]
	s_add_i32 s4, s51, s96
	s_add_i32 s4, s4, s96
	s_cmp_gt_i32 s4, 0x179ff
	s_cbranch_scc0 .Lwd_two
	s_waitcnt vmcnt(0)
	s_add_u32 s20, s30, s16
	s_addc_u32 s21, s31, 0
	v_add_u32_e32 v209, 0x1000, v19
	v_add_u32_e32 v210, 0x1400, v19
	v_add_u32_e32 v211, 0x1800, v19
	v_add_u32_e32 v212, 0x1c00, v19
	v_mul_f32_e32 v144, 0x43000000, v144
	v_mul_f32_e32 v145, 0x43000000, v145
	ds_write2_b32 v19, v144, v145 offset1:66
	v_mul_f32_e32 v146, 0x43000000, v146
	v_mul_f32_e32 v147, 0x43000000, v147
	ds_write2_b32 v19, v146, v147 offset0:132 offset1:198
	v_mul_f32_e32 v148, 0x43000000, v148
	v_mul_f32_e32 v149, 0x43000000, v149
	ds_write2_b32 v61, v148, v149 offset0:8 offset1:74
	v_mul_f32_e32 v150, 0x43000000, v150
	v_mul_f32_e32 v151, 0x43000000, v151
	ds_write2_b32 v61, v150, v151 offset0:140 offset1:206
	v_mul_f32_e32 v152, 0x43000000, v152
	v_mul_f32_e32 v153, 0x43000000, v153
	ds_write2_b32 v62, v152, v153 offset0:16 offset1:82
	v_mul_f32_e32 v154, 0x43000000, v154
	v_mul_f32_e32 v155, 0x43000000, v155
	ds_write2_b32 v62, v154, v155 offset0:148 offset1:214
	v_mul_f32_e32 v156, 0x43000000, v156
	v_mul_f32_e32 v157, 0x43000000, v157
	ds_write2_b32 v63, v156, v157 offset0:24 offset1:90
	v_mul_f32_e32 v158, 0x43000000, v158
	v_mul_f32_e32 v159, 0x43000000, v159
	ds_write2_b32 v63, v158, v159 offset0:156 offset1:222
	v_mul_f32_e32 v160, 0x43000000, v160
	v_mul_f32_e32 v161, 0x43000000, v161
	ds_write2_b32 v209, v160, v161 offset0:32 offset1:98
	v_mul_f32_e32 v162, 0x43000000, v162
	v_mul_f32_e32 v163, 0x43000000, v163
	ds_write2_b32 v209, v162, v163 offset0:164 offset1:230
	v_mul_f32_e32 v164, 0x43000000, v164
	v_mul_f32_e32 v165, 0x43000000, v165
	ds_write2_b32 v210, v164, v165 offset0:40 offset1:106
	v_mul_f32_e32 v166, 0x43000000, v166
	v_mul_f32_e32 v167, 0x43000000, v167
	ds_write2_b32 v210, v166, v167 offset0:172 offset1:238
	v_mul_f32_e32 v168, 0x43000000, v168
	v_mul_f32_e32 v169, 0x43000000, v169
	ds_write2_b32 v211, v168, v169 offset0:48 offset1:114
	v_mul_f32_e32 v170, 0x43000000, v170
	v_mul_f32_e32 v171, 0x43000000, v171
	ds_write2_b32 v211, v170, v171 offset0:180 offset1:246
	v_mul_f32_e32 v172, 0x43000000, v172
	v_mul_f32_e32 v173, 0x43000000, v173
	ds_write2_b32 v212, v172, v173 offset0:56 offset1:122
	v_mul_f32_e32 v174, 0x43000000, v174
	v_mul_f32_e32 v175, 0x43000000, v175
	ds_write2_b32 v212, v174, v175 offset0:188 offset1:254
	s_waitcnt lgkmcnt(0)
; #define GAS __attribute__((address_space(1)))
; #define LAS __attribute__((address_space(3)))
; #define LDS_WAIT() asm volatile("s_waitcnt lgkmcnt(0)" ::: "memory")
;     const int pr = item >> 1, kb = 2 * (pr / nblk) + (item & 1), nb = pr % nblk, k0 = 64 * kb, n0 = 32 * nb;
;     const int nr = n0 + (lane & 31); const int sc = MAP == 1 ? src_col_in(nr) : nr;
;     float v[32];
; #pragma unroll
;     for (int i = 0; i < 32; ++i) v[i] = sc >= 0 ? W[(size_t)(k0 + 2 * i + (lane >> 5)) * Nsrc + sc] : 0.f;
; #pragma unroll
;     for (int i = 0; i < 32; ++i) { const int k = k0 + 2 * i + (lane >> 5); float x = v[i] * wscale; if (KS) x *= (k < ksplit ? ksA[k] : ksB[k - ksplit]); scr[(2 * i + (lane >> 5)) * 33 + (lane & 31)] = x; }
;     LDS_WAIT(); asm volatile("" ::: "memory");
;     const int c = lane & 7;
; #pragma unroll
;     for (int j = 0; j < 4; ++j) { const int n = (lane >> 3) + 8 * j; const LAS float* s = scr + (8 * c) * 33 + n;
;         const unsigned long long o = (unsigned long long)pg8::pk4_fp8(s[0 * 33], s[1 * 33], s[2 * 33], s[3 * 33]) | ((unsigned long long)pg8::pk4_fp8(s[4 * 33], s[5 * 33], s[6 * 33], s[7 * 33]) << 32);
;         *(GAS unsigned long long*)(WT + (size_t)(n0 + n) * K + k0 + 8 * c) = o; }
;     LDS_WAIT(); asm volatile("" ::: "memory");
; }
	ds_read2_b32 v[214:215], v21 offset1:8
	ds_read2_b32 v[216:217], v21 offset0:33 offset1:41
	ds_read2_b32 v[218:219], v21 offset0:66 offset1:74
	ds_read2_b32 v[220:221], v21 offset0:99 offset1:107
	ds_read2_b32 v[222:223], v21 offset0:132 offset1:140
	ds_read2_b32 v[224:225], v21 offset0:165 offset1:173
	ds_read2_b32 v[226:227], v21 offset0:198 offset1:206
	ds_read2_b32 v[228:229], v21 offset0:231 offset1:239
	s_waitcnt lgkmcnt(0)
	v_max_f32_e32 v214, v214, v214
	v_max_f32_e32 v216, v216, v216
	v_max_f32_e32 v218, v218, v218
	v_max_f32_e32 v220, v220, v220
	v_max_f32_e32 v222, v222, v222
	v_max_f32_e32 v224, v224, v224
	v_max_f32_e32 v226, v226, v226
	v_max_f32_e32 v228, v228, v228
	v_med3_f32 v214, v214, s44, v64
	v_med3_f32 v216, v216, s44, v64
	v_med3_f32 v218, v218, s44, v64
	v_med3_f32 v220, v220, s44, v64
	v_med3_f32 v222, v222, s44, v64
	v_med3_f32 v224, v224, s44, v64
	v_med3_f32 v226, v226, s44, v64
	v_med3_f32 v228, v228, s44, v64
	v_mov_b32_e32 v230, v11
	v_mov_b32_e32 v231, v11
	v_or_b32_e32 v233, s36, v20
	v_cvt_pk_fp8_f32 v230, v214, v216
	v_cvt_pk_fp8_f32 v231, v222, v224
	v_lshl_add_u32 v232, v233, 14, v8
	v_cvt_pk_fp8_f32 v230, v218, v220 op_sel:[0,0,1]
	v_cvt_pk_fp8_f32 v231, v226, v228 op_sel:[0,0,1]
	s_nop 0
	global_store_dwordx2 v232, v[230:231], s[20:21]
	s_nop 1
	v_max_f32_e32 v215, v215, v215
	v_max_f32_e32 v217, v217, v217
	v_max_f32_e32 v219, v219, v219
	v_max_f32_e32 v221, v221, v221
	v_max_f32_e32 v223, v223, v223
	v_max_f32_e32 v225, v225, v225
	v_max_f32_e32 v227, v227, v227
	v_max_f32_e32 v229, v229, v229
	v_med3_f32 v215, v215, s44, v64
	v_med3_f32 v217, v217, s44, v64
	v_med3_f32 v219, v219, s44, v64
	v_med3_f32 v221, v221, s44, v64
	v_med3_f32 v223, v223, s44, v64
	v_med3_f32 v225, v225, s44, v64
	v_med3_f32 v227, v227, s44, v64
	v_med3_f32 v229, v229, s44, v64
	v_mov_b32_e32 v230, v11
	v_mov_b32_e32 v231, v11
	v_or_b32_e32 v233, s36, v22
	v_cvt_pk_fp8_f32 v230, v215, v217
	v_cvt_pk_fp8_f32 v231, v223, v225
	v_lshl_add_u32 v232, v233, 14, v8
	v_cvt_pk_fp8_f32 v230, v219, v221 op_sel:[0,0,1]
	v_cvt_pk_fp8_f32 v231, v227, v229 op_sel:[0,0,1]
	s_nop 0
	global_store_dwordx2 v232, v[230:231], s[20:21]
	s_nop 1
	ds_read2_b32 v[214:215], v21 offset0:16 offset1:24
	ds_read2_b32 v[216:217], v21 offset0:49 offset1:57
	ds_read2_b32 v[218:219], v21 offset0:82 offset1:90
	ds_read2_b32 v[220:221], v21 offset0:115 offset1:123
	ds_read2_b32 v[222:223], v21 offset0:148 offset1:156
	ds_read2_b32 v[224:225], v21 offset0:181 offset1:189
	ds_read2_b32 v[226:227], v21 offset0:214 offset1:222
	ds_read2_b32 v[228:229], v21 offset0:247 offset1:255
	s_waitcnt lgkmcnt(0)
	v_max_f32_e32 v214, v214, v214
	v_max_f32_e32 v216, v216, v216
	v_max_f32_e32 v218, v218, v218
	v_max_f32_e32 v220, v220, v220
	v_max_f32_e32 v222, v222, v222
	v_max_f32_e32 v224, v224, v224
	v_max_f32_e32 v226, v226, v226
	v_max_f32_e32 v228, v228, v228
	v_med3_f32 v214, v214, s44, v64
	v_med3_f32 v216, v216, s44, v64
	v_med3_f32 v218, v218, s44, v64
	v_med3_f32 v220, v220, s44, v64
	v_med3_f32 v222, v222, s44, v64
	v_med3_f32 v224, v224, s44, v64
	v_med3_f32 v226, v226, s44, v64
	v_med3_f32 v228, v228, s44, v64
	v_mov_b32_e32 v230, v11
	v_mov_b32_e32 v231, v11
	v_or_b32_e32 v233, s36, v23
	v_cvt_pk_fp8_f32 v230, v214, v216
	v_cvt_pk_fp8_f32 v231, v222, v224
	v_lshl_add_u32 v232, v233, 14, v8
	v_cvt_pk_fp8_f32 v230, v218, v220 op_sel:[0,0,1]
	v_cvt_pk_fp8_f32 v231, v226, v228 op_sel:[0,0,1]
	s_nop 0
	global_store_dwordx2 v232, v[230:231], s[20:21]
	s_nop 1
	v_max_f32_e32 v215, v215, v215
	v_max_f32_e32 v217, v217, v217
	v_max_f32_e32 v219, v219, v219
	v_max_f32_e32 v221, v221, v221
	v_max_f32_e32 v223, v223, v223
	v_max_f32_e32 v225, v225, v225
	v_max_f32_e32 v227, v227, v227
	v_max_f32_e32 v229, v229, v229
	v_med3_f32 v215, v215, s44, v64
	v_med3_f32 v217, v217, s44, v64
	v_med3_f32 v219, v219, s44, v64
	v_med3_f32 v221, v221, s44, v64
	v_med3_f32 v223, v223, s44, v64
	v_med3_f32 v225, v225, s44, v64
	v_med3_f32 v227, v227, s44, v64
	v_med3_f32 v229, v229, s44, v64
	v_mov_b32_e32 v230, v11
	v_mov_b32_e32 v231, v11
	v_or_b32_e32 v233, s36, v24
	v_cvt_pk_fp8_f32 v230, v215, v217
	v_cvt_pk_fp8_f32 v231, v223, v225
	v_lshl_add_u32 v232, v233, 14, v8
	v_cvt_pk_fp8_f32 v230, v219, v221 op_sel:[0,0,1]
	v_cvt_pk_fp8_f32 v231, v227, v229 op_sel:[0,0,1]
	s_nop 0
	global_store_dwordx2 v232, v[230:231], s[20:21]
	s_nop 1
	s_waitcnt lgkmcnt(0)
	s_add_i32 s50, s50, s96
	s_add_i32 s39, s39, s76
	s_add_i32 s40, s40, s41
	s_add_i32 s42, s42, s43
	s_add_i32 s51, s51, s96
	s_branch .Lwd_orig
; #define GAS __attribute__((address_space(1)))
; #define LAS __attribute__((address_space(3)))
;     const int pr = item >> 1, kb = 2 * (pr / nblk) + (item & 1), nb = pr % nblk, k0 = 64 * kb, n0 = 32 * nb;
;     const int nr = n0 + (lane & 31); const int sc = MAP == 1 ? src_col_in(nr) : nr;
;     float v[32];
; #pragma unroll
;     for (int i = 0; i < 32; ++i) v[i] = sc >= 0 ? W[(size_t)(k0 + 2 * i + (lane >> 5)) * Nsrc + sc] : 0.f;
; #pragma unroll
;     for (int i = 0; i < 32; ++i) { const int k = k0 + 2 * i + (lane >> 5); float x = v[i] * wscale; if (KS) x *= (k < ksplit ? ksA[k] : ksB[k - ksplit]); scr[(2 * i + (lane >> 5)) * 33 + (lane & 31)] = x; }
;     LDS_WAIT(); asm volatile("" ::: "memory");
;     const int c = lane & 7;
; #pragma unroll
;     for (int j = 0; j < 4; ++j) { const int n = (lane >> 3) + 8 * j; const LAS float* s = scr + (8 * c) * 33 + n;
;         const unsigned long long o = (unsigned long long)pg8::pk4_fp8(s[0 * 33], s[1 * 33], s[2 * 33], s[3 * 33]) | ((unsigned long long)pg8::pk4_fp8(s[4 * 33], s[5 * 33], s[6 * 33], s[7 * 33]) << 32);
;         *(GAS unsigned long long*)(WT + (size_t)(n0 + n) * K + k0 + 8 * c) = o; }
;     LDS_WAIT(); asm volatile("" ::: "memory");
; }
; __global__ void __launch_bounds__(NWAVES * 64, 2) hybrid_fwd(Args args) {
;     ...
;         for (int it = gw; it < DEPTH * I_L; it += NGW) {
;             const int l = it / I_L; int r = it % I_L;
;             if (r < I_IN) { if (l >= PROJ_F8_FROM) p0_transpose_item_f8<true, 1>(args.in[2] + (size_t)l * DM * NSRC, DM, NSRC, NPROJ / 32, (unsigned char*)(ws + WS_WIN + l * SZ_WIN), WUP8_SCALE, args.in[1] + l * DM, args.in[1] + l * DM, DM, scr, r, lane);
;                 else p0_transpose_item<1, true>(args.in[2] + (size_t)l * DM * NSRC, DM, NSRC, NPROJ / 32, (bf16*)(ws + WS_WIN + l * SZ_WIN), args.in[1] + l * DM, args.in[1] + l * DM, DM, scr, r, lane); continue; } r -= I_IN;
;             if (r < I_O) { if (l >= WO_F8_FROM) p0_transpose_item_f8<true>(args.in[13] + (size_t)l * DM * DM, DM, DM, DM / 32, (unsigned char*)(ws + WS_WO + l * SZ_WO), 64.f, args.in[6] + l * 2048, args.in[12] + l * 2048, 2048, scr, r, lane);
;                 else p0_transpose_item<0, true>(args.in[13] + (size_t)l * DM * DM, DM, DM, DM / 32, (bf16*)(ws + WS_WO + l * SZ_WO), args.in[6] + l * 2048, args.in[12] + l * 2048, 2048, scr, r, lane); continue; } r -= I_O;
.Lwd_two:
	s_add_i32 s50, s50, s96
	s_add_i32 s39, s39, s76
	s_add_i32 s40, s40, s41
	s_add_i32 s42, s42, s43
	s_add_i32 s51, s51, s96
	s_add_i32 s20, s51, 0xffff0600
	s_lshr_b32 s4, s20, 7
	s_and_b32 s4, s4, 0xfe
	s_and_b32 s5, s20, 1
	s_or_b32 s4, s4, s5
	s_lshl_b32 s4, s4, 6
	s_lshl_b32 s5, s20, 4
	s_and_b32 s5, s5, 0xfe0
	v_or_b32_e32 v208, s4, v6
	v_lshlrev_b32_e32 v208, 12, v208
	v_or3_b32 v208, s5, v18, v208
	v_lshlrev_b32_e32 v208, 2, v208
	s_mov_b64 s[8:9], s[10:11]
	global_load_dword v176, v208, s[8:9]
	s_add_u32 s8, s8, 0x8000
	s_addc_u32 s9, s9, 0
	global_load_dword v177, v208, s[8:9]
	s_add_u32 s8, s8, 0x8000
	s_addc_u32 s9, s9, 0
	global_load_dword v178, v208, s[8:9]
	s_add_u32 s8, s8, 0x8000
	s_addc_u32 s9, s9, 0
	global_load_dword v179, v208, s[8:9]
	s_add_u32 s8, s8, 0x8000
	s_addc_u32 s9, s9, 0
	global_load_dword v180, v208, s[8:9]
	s_add_u32 s8, s8, 0x8000
	s_addc_u32 s9, s9, 0
	global_load_dword v181, v208, s[8:9]
	s_add_u32 s8, s8, 0x8000
	s_addc_u32 s9, s9, 0
	global_load_dword v182, v208, s[8:9]
	s_add_u32 s8, s8, 0x8000
	s_addc_u32 s9, s9, 0
	global_load_dword v183, v208, s[8:9]
	s_add_u32 s8, s8, 0x8000
	s_addc_u32 s9, s9, 0
	global_load_dword v184, v208, s[8:9]
	s_add_u32 s8, s8, 0x8000
	s_addc_u32 s9, s9, 0
	global_load_dword v185, v208, s[8:9]
	s_add_u32 s8, s8, 0x8000
	s_addc_u32 s9, s9, 0
	global_load_dword v186, v208, s[8:9]
	s_add_u32 s8, s8, 0x8000
	s_addc_u32 s9, s9, 0
	global_load_dword v187, v208, s[8:9]
	s_add_u32 s8, s8, 0x8000
	s_addc_u32 s9, s9, 0
	global_load_dword v188, v208, s[8:9]
	s_add_u32 s8, s8, 0x8000
	s_addc_u32 s9, s9, 0
	global_load_dword v189, v208, s[8:9]
	s_add_u32 s8, s8, 0x8000
	s_addc_u32 s9, s9, 0
	global_load_dword v190, v208, s[8:9]
	s_add_u32 s8, s8, 0x8000
	s_addc_u32 s9, s9, 0
	global_load_dword v191, v208, s[8:9]
	s_add_u32 s8, s8, 0x8000
	s_addc_u32 s9, s9, 0
	global_load_dword v192, v208, s[8:9]
	s_add_u32 s8, s8, 0x8000
	s_addc_u32 s9, s9, 0
	global_load_dword v193, v208, s[8:9]
	s_add_u32 s8, s8, 0x8000
	s_addc_u32 s9, s9, 0
	global_load_dword v194, v208, s[8:9]
	s_add_u32 s8, s8, 0x8000
	s_addc_u32 s9, s9, 0
	global_load_dword v195, v208, s[8:9]
	s_add_u32 s8, s8, 0x8000
	s_addc_u32 s9, s9, 0
	global_load_dword v196, v208, s[8:9]
	s_add_u32 s8, s8, 0x8000
	s_addc_u32 s9, s9, 0
	global_load_dword v197, v208, s[8:9]
	s_add_u32 s8, s8, 0x8000
	s_addc_u32 s9, s9, 0
	global_load_dword v198, v208, s[8:9]
	s_add_u32 s8, s8, 0x8000
	s_addc_u32 s9, s9, 0
	global_load_dword v199, v208, s[8:9]
	s_add_u32 s8, s8, 0x8000
	s_addc_u32 s9, s9, 0
	global_load_dword v200, v208, s[8:9]
	s_add_u32 s8, s8, 0x8000
	s_addc_u32 s9, s9, 0
	global_load_dword v201, v208, s[8:9]
	s_add_u32 s8, s8, 0x8000
	s_addc_u32 s9, s9, 0
	global_load_dword v202, v208, s[8:9]
	s_add_u32 s8, s8, 0x8000
	s_addc_u32 s9, s9, 0
	global_load_dword v203, v208, s[8:9]
	s_add_u32 s8, s8, 0x8000
	s_addc_u32 s9, s9, 0
	global_load_dword v204, v208, s[8:9]
	s_add_u32 s8, s8, 0x8000
	s_addc_u32 s9, s9, 0
	global_load_dword v205, v208, s[8:9]
	s_add_u32 s8, s8, 0x8000
	s_addc_u32 s9, s9, 0
	global_load_dword v206, v208, s[8:9]
	s_add_u32 s8, s8, 0x8000
	s_addc_u32 s9, s9, 0
	global_load_dword v207, v208, s[8:9]
	s_waitcnt vmcnt(32)
	s_add_u32 s20, s30, s16
	s_addc_u32 s21, s31, 0
	v_add_u32_e32 v209, 0x1000, v19
	v_add_u32_e32 v210, 0x1400, v19
	v_add_u32_e32 v211, 0x1800, v19
	v_add_u32_e32 v212, 0x1c00, v19
	v_mul_f32_e32 v144, 0x43000000, v144
	v_mul_f32_e32 v145, 0x43000000, v145
	ds_write2_b32 v19, v144, v145 offset1:66
	v_mul_f32_e32 v146, 0x43000000, v146
	v_mul_f32_e32 v147, 0x43000000, v147
	ds_write2_b32 v19, v146, v147 offset0:132 offset1:198
	v_mul_f32_e32 v148, 0x43000000, v148
	v_mul_f32_e32 v149, 0x43000000, v149
	ds_write2_b32 v61, v148, v149 offset0:8 offset1:74
	v_mul_f32_e32 v150, 0x43000000, v150
	v_mul_f32_e32 v151, 0x43000000, v151
	ds_write2_b32 v61, v150, v151 offset0:140 offset1:206
	v_mul_f32_e32 v152, 0x43000000, v152
	v_mul_f32_e32 v153, 0x43000000, v153
	ds_write2_b32 v62, v152, v153 offset0:16 offset1:82
	v_mul_f32_e32 v154, 0x43000000, v154
	v_mul_f32_e32 v155, 0x43000000, v155
	ds_write2_b32 v62, v154, v155 offset0:148 offset1:214
	v_mul_f32_e32 v156, 0x43000000, v156
	v_mul_f32_e32 v157, 0x43000000, v157
	ds_write2_b32 v63, v156, v157 offset0:24 offset1:90
	v_mul_f32_e32 v158, 0x43000000, v158
	v_mul_f32_e32 v159, 0x43000000, v159
	ds_write2_b32 v63, v158, v159 offset0:156 offset1:222
	v_mul_f32_e32 v160, 0x43000000, v160
	v_mul_f32_e32 v161, 0x43000000, v161
	ds_write2_b32 v209, v160, v161 offset0:32 offset1:98
	v_mul_f32_e32 v162, 0x43000000, v162
	v_mul_f32_e32 v163, 0x43000000, v163
	ds_write2_b32 v209, v162, v163 offset0:164 offset1:230
	v_mul_f32_e32 v164, 0x43000000, v164
	v_mul_f32_e32 v165, 0x43000000, v165
	ds_write2_b32 v210, v164, v165 offset0:40 offset1:106
	v_mul_f32_e32 v166, 0x43000000, v166
	v_mul_f32_e32 v167, 0x43000000, v167
	ds_write2_b32 v210, v166, v167 offset0:172 offset1:238
	v_mul_f32_e32 v168, 0x43000000, v168
	v_mul_f32_e32 v169, 0x43000000, v169
	ds_write2_b32 v211, v168, v169 offset0:48 offset1:114
	v_mul_f32_e32 v170, 0x43000000, v170
	v_mul_f32_e32 v171, 0x43000000, v171
	ds_write2_b32 v211, v170, v171 offset0:180 offset1:246
	v_mul_f32_e32 v172, 0x43000000, v172
	v_mul_f32_e32 v173, 0x43000000, v173
	ds_write2_b32 v212, v172, v173 offset0:56 offset1:122
	v_mul_f32_e32 v174, 0x43000000, v174
	v_mul_f32_e32 v175, 0x43000000, v175
	ds_write2_b32 v212, v174, v175 offset0:188 offset1:254
	s_waitcnt lgkmcnt(0)
; #define GAS __attribute__((address_space(1)))
; #define LAS __attribute__((address_space(3)))
; #define LDS_WAIT() asm volatile("s_waitcnt lgkmcnt(0)" ::: "memory")
;     const int pr = item >> 1, kb = 2 * (pr / nblk) + (item & 1), nb = pr % nblk, k0 = 64 * kb, n0 = 32 * nb;
;     const int nr = n0 + (lane & 31); const int sc = MAP == 1 ? src_col_in(nr) : nr;
;     float v[32];
; #pragma unroll
;     for (int i = 0; i < 32; ++i) v[i] = sc >= 0 ? W[(size_t)(k0 + 2 * i + (lane >> 5)) * Nsrc + sc] : 0.f;
; #pragma unroll
;     for (int i = 0; i < 32; ++i) { const int k = k0 + 2 * i + (lane >> 5); float x = v[i] * wscale; if (KS) x *= (k < ksplit ? ksA[k] : ksB[k - ksplit]); scr[(2 * i + (lane >> 5)) * 33 + (lane & 31)] = x; }
;     LDS_WAIT(); asm volatile("" ::: "memory");
;     const int c = lane & 7;
; #pragma unroll
;     for (int j = 0; j < 4; ++j) { const int n = (lane >> 3) + 8 * j; const LAS float* s = scr + (8 * c) * 33 + n;
;         const unsigned long long o = (unsigned long long)pg8::pk4_fp8(s[0 * 33], s[1 * 33], s[2 * 33], s[3 * 33]) | ((unsigned long long)pg8::pk4_fp8(s[4 * 33], s[5 * 33], s[6 * 33], s[7 * 33]) << 32);
;         *(GAS unsigned long long*)(WT + (size_t)(n0 + n) * K + k0 + 8 * c) = o; }
;     LDS_WAIT(); asm volatile("" ::: "memory");
; }
	ds_read2_b32 v[214:215], v21 offset1:8
	ds_read2_b32 v[216:217], v21 offset0:33 offset1:41
	ds_read2_b32 v[218:219], v21 offset0:66 offset1:74
	ds_read2_b32 v[220:221], v21 offset0:99 offset1:107
	ds_read2_b32 v[222:223], v21 offset0:132 offset1:140
	ds_read2_b32 v[224:225], v21 offset0:165 offset1:173
	ds_read2_b32 v[226:227], v21 offset0:198 offset1:206
	ds_read2_b32 v[228:229], v21 offset0:231 offset1:239
	s_waitcnt lgkmcnt(0)
	v_max_f32_e32 v214, v214, v214
	v_max_f32_e32 v216, v216, v216
	v_max_f32_e32 v218, v218, v218
	v_max_f32_e32 v220, v220, v220
	v_max_f32_e32 v222, v222, v222
	v_max_f32_e32 v224, v224, v224
	v_max_f32_e32 v226, v226, v226
	v_max_f32_e32 v228, v228, v228
	v_med3_f32 v214, v214, s44, v64
	v_med3_f32 v216, v216, s44, v64
	v_med3_f32 v218, v218, s44, v64
	v_med3_f32 v220, v220, s44, v64
	v_med3_f32 v222, v222, s44, v64
	v_med3_f32 v224, v224, s44, v64
	v_med3_f32 v226, v226, s44, v64
	v_med3_f32 v228, v228, s44, v64
	v_mov_b32_e32 v230, v11
	v_mov_b32_e32 v231, v11
	v_or_b32_e32 v233, s36, v20
	v_cvt_pk_fp8_f32 v230, v214, v216
	v_cvt_pk_fp8_f32 v231, v222, v224
	v_lshl_add_u32 v232, v233, 14, v8
	v_cvt_pk_fp8_f32 v230, v218, v220 op_sel:[0,0,1]
	v_cvt_pk_fp8_f32 v231, v226, v228 op_sel:[0,0,1]
	s_nop 0
	global_store_dwordx2 v232, v[230:231], s[20:21]
	s_nop 1
	v_max_f32_e32 v215, v215, v215
	v_max_f32_e32 v217, v217, v217
	v_max_f32_e32 v219, v219, v219
	v_max_f32_e32 v221, v221, v221
	v_max_f32_e32 v223, v223, v223
	v_max_f32_e32 v225, v225, v225
	v_max_f32_e32 v227, v227, v227
	v_max_f32_e32 v229, v229, v229
	v_med3_f32 v215, v215, s44, v64
	v_med3_f32 v217, v217, s44, v64
	v_med3_f32 v219, v219, s44, v64
	v_med3_f32 v221, v221, s44, v64
	v_med3_f32 v223, v223, s44, v64
	v_med3_f32 v225, v225, s44, v64
	v_med3_f32 v227, v227, s44, v64
	v_med3_f32 v229, v229, s44, v64
	v_mov_b32_e32 v230, v11
	v_mov_b32_e32 v231, v11
	v_or_b32_e32 v233, s36, v22
	v_cvt_pk_fp8_f32 v230, v215, v217
	v_cvt_pk_fp8_f32 v231, v223, v225
	v_lshl_add_u32 v232, v233, 14, v8
	v_cvt_pk_fp8_f32 v230, v219, v221 op_sel:[0,0,1]
	v_cvt_pk_fp8_f32 v231, v227, v229 op_sel:[0,0,1]
	s_nop 0
	global_store_dwordx2 v232, v[230:231], s[20:21]
	s_nop 1
	ds_read2_b32 v[214:215], v21 offset0:16 offset1:24
	ds_read2_b32 v[216:217], v21 offset0:49 offset1:57
	ds_read2_b32 v[218:219], v21 offset0:82 offset1:90
	ds_read2_b32 v[220:221], v21 offset0:115 offset1:123
	ds_read2_b32 v[222:223], v21 offset0:148 offset1:156
	ds_read2_b32 v[224:225], v21 offset0:181 offset1:189
	ds_read2_b32 v[226:227], v21 offset0:214 offset1:222
	ds_read2_b32 v[228:229], v21 offset0:247 offset1:255
	s_waitcnt lgkmcnt(0)
	v_max_f32_e32 v214, v214, v214
	v_max_f32_e32 v216, v216, v216
	v_max_f32_e32 v218, v218, v218
	v_max_f32_e32 v220, v220, v220
	v_max_f32_e32 v222, v222, v222
	v_max_f32_e32 v224, v224, v224
	v_max_f32_e32 v226, v226, v226
	v_max_f32_e32 v228, v228, v228
	v_med3_f32 v214, v214, s44, v64
	v_med3_f32 v216, v216, s44, v64
	v_med3_f32 v218, v218, s44, v64
	v_med3_f32 v220, v220, s44, v64
	v_med3_f32 v222, v222, s44, v64
	v_med3_f32 v224, v224, s44, v64
	v_med3_f32 v226, v226, s44, v64
	v_med3_f32 v228, v228, s44, v64
	v_mov_b32_e32 v230, v11
	v_mov_b32_e32 v231, v11
	v_or_b32_e32 v233, s36, v23
	v_cvt_pk_fp8_f32 v230, v214, v216
	v_cvt_pk_fp8_f32 v231, v222, v224
	v_lshl_add_u32 v232, v233, 14, v8
	v_cvt_pk_fp8_f32 v230, v218, v220 op_sel:[0,0,1]
	v_cvt_pk_fp8_f32 v231, v226, v228 op_sel:[0,0,1]
	s_nop 0
	global_store_dwordx2 v232, v[230:231], s[20:21]
	s_nop 1
	v_max_f32_e32 v215, v215, v215
	v_max_f32_e32 v217, v217, v217
	v_max_f32_e32 v219, v219, v219
	v_max_f32_e32 v221, v221, v221
	v_max_f32_e32 v223, v223, v223
	v_max_f32_e32 v225, v225, v225
	v_max_f32_e32 v227, v227, v227
	v_max_f32_e32 v229, v229, v229
	v_med3_f32 v215, v215, s44, v64
	v_med3_f32 v217, v217, s44, v64
	v_med3_f32 v219, v219, s44, v64
	v_med3_f32 v221, v221, s44, v64
	v_med3_f32 v223, v223, s44, v64
	v_med3_f32 v225, v225, s44, v64
	v_med3_f32 v227, v227, s44, v64
	v_med3_f32 v229, v229, s44, v64
	v_mov_b32_e32 v230, v11
	v_mov_b32_e32 v231, v11
	v_or_b32_e32 v233, s36, v24
	v_cvt_pk_fp8_f32 v230, v215, v217
	v_cvt_pk_fp8_f32 v231, v223, v225
	v_lshl_add_u32 v232, v233, 14, v8
	v_cvt_pk_fp8_f32 v230, v219, v221 op_sel:[0,0,1]
	v_cvt_pk_fp8_f32 v231, v227, v229 op_sel:[0,0,1]
	s_nop 0
	global_store_dwordx2 v232, v[230:231], s[20:21]
	s_nop 1
	s_waitcnt lgkmcnt(0)
	s_mov_b32 s16, s4
	s_mov_b32 s36, s5
; #define GAS __attribute__((address_space(1)))
; #define LAS __attribute__((address_space(3)))
;     const int pr = item >> 1, kb = 2 * (pr / nblk) + (item & 1), nb = pr % nblk, k0 = 64 * kb, n0 = 32 * nb;
;     const int nr = n0 + (lane & 31); const int sc = MAP == 1 ? src_col_in(nr) : nr;
;     float v[32];
; #pragma unroll
;     for (int i = 0; i < 32; ++i) v[i] = sc >= 0 ? W[(size_t)(k0 + 2 * i + (lane >> 5)) * Nsrc + sc] : 0.f;
; #pragma unroll
;     for (int i = 0; i < 32; ++i) { const int k = k0 + 2 * i + (lane >> 5); float x = v[i] * wscale; if (KS) x *= (k < ksplit ? ksA[k] : ksB[k - ksplit]); scr[(2 * i + (lane >> 5)) * 33 + (lane & 31)] = x; }
;     LDS_WAIT(); asm volatile("" ::: "memory");
;     const int c = lane & 7;
; #pragma unroll
;     for (int j = 0; j < 4; ++j) { const int n = (lane >> 3) + 8 * j; const LAS float* s = scr + (8 * c) * 33 + n;
;         const unsigned long long o = (unsigned long long)pg8::pk4_fp8(s[0 * 33], s[1 * 33], s[2 * 33], s[3 * 33]) | ((unsigned long long)pg8::pk4_fp8(s[4 * 33], s[5 * 33], s[6 * 33], s[7 * 33]) << 32);
;         *(GAS unsigned long long*)(WT + (size_t)(n0 + n) * K + k0 + 8 * c) = o; }
;     LDS_WAIT(); asm volatile("" ::: "memory");
; }
; __global__ void __launch_bounds__(NWAVES * 64, 2) hybrid_fwd(Args args) {
;     ...
;         for (int it = gw; it < DEPTH * I_L; it += NGW) {
;             const int l = it / I_L; int r = it % I_L;
;             if (r < I_IN) { if (l >= PROJ_F8_FROM) p0_transpose_item_f8<true, 1>(args.in[2] + (size_t)l * DM * NSRC, DM, NSRC, NPROJ / 32, (unsigned char*)(ws + WS_WIN + l * SZ_WIN), WUP8_SCALE, args.in[1] + l * DM, args.in[1] + l * DM, DM, scr, r, lane);
;                 else p0_transpose_item<1, true>(args.in[2] + (size_t)l * DM * NSRC, DM, NSRC, NPROJ / 32, (bf16*)(ws + WS_WIN + l * SZ_WIN), args.in[1] + l * DM, args.in[1] + l * DM, DM, scr, r, lane); continue; } r -= I_IN;
;             if (r < I_O) { if (l >= WO_F8_FROM) p0_transpose_item_f8<true>(args.in[13] + (size_t)l * DM * DM, DM, DM, DM / 32, (unsigned char*)(ws + WS_WO + l * SZ_WO), 64.f, args.in[6] + l * 2048, args.in[12] + l * 2048, 2048, scr, r, lane);
;                 else p0_transpose_item<0, true>(args.in[13] + (size_t)l * DM * DM, DM, DM, DM / 32, (bf16*)(ws + WS_WO + l * SZ_WO), args.in[6] + l * 2048, args.in[12] + l * 2048, 2048, scr, r, lane); continue; } r -= I_O;
.Lwd_loopY:
	s_add_i32 s4, s51, s96
	s_add_i32 s4, s4, s96
	s_cmp_gt_i32 s4, 0x179ff
	s_cbranch_scc0 .Lwd_loopY_more
	s_waitcnt vmcnt(4)
	s_add_u32 s20, s30, s16
	s_addc_u32 s21, s31, 0
	v_add_u32_e32 v209, 0x1000, v19
	v_add_u32_e32 v210, 0x1400, v19
	v_add_u32_e32 v211, 0x1800, v19
	v_add_u32_e32 v212, 0x1c00, v19
	v_mul_f32_e32 v176, 0x43000000, v176
	v_mul_f32_e32 v177, 0x43000000, v177
	ds_write2_b32 v19, v176, v177 offset1:66
	v_mul_f32_e32 v178, 0x43000000, v178
	v_mul_f32_e32 v179, 0x43000000, v179
	ds_write2_b32 v19, v178, v179 offset0:132 offset1:198
	v_mul_f32_e32 v180, 0x43000000, v180
	v_mul_f32_e32 v181, 0x43000000, v181
	ds_write2_b32 v61, v180, v181 offset0:8 offset1:74
	v_mul_f32_e32 v182, 0x43000000, v182
	v_mul_f32_e32 v183, 0x43000000, v183
	ds_write2_b32 v61, v182, v183 offset0:140 offset1:206
	v_mul_f32_e32 v184, 0x43000000, v184
	v_mul_f32_e32 v185, 0x43000000, v185
	ds_write2_b32 v62, v184, v185 offset0:16 offset1:82
	v_mul_f32_e32 v186, 0x43000000, v186
	v_mul_f32_e32 v187, 0x43000000, v187
	ds_write2_b32 v62, v186, v187 offset0:148 offset1:214
	v_mul_f32_e32 v188, 0x43000000, v188
	v_mul_f32_e32 v189, 0x43000000, v189
	ds_write2_b32 v63, v188, v189 offset0:24 offset1:90
	v_mul_f32_e32 v190, 0x43000000, v190
	v_mul_f32_e32 v191, 0x43000000, v191
	ds_write2_b32 v63, v190, v191 offset0:156 offset1:222
	v_mul_f32_e32 v192, 0x43000000, v192
	v_mul_f32_e32 v193, 0x43000000, v193
	ds_write2_b32 v209, v192, v193 offset0:32 offset1:98
	v_mul_f32_e32 v194, 0x43000000, v194
	v_mul_f32_e32 v195, 0x43000000, v195
	ds_write2_b32 v209, v194, v195 offset0:164 offset1:230
	v_mul_f32_e32 v196, 0x43000000, v196
	v_mul_f32_e32 v197, 0x43000000, v197
	ds_write2_b32 v210, v196, v197 offset0:40 offset1:106
	v_mul_f32_e32 v198, 0x43000000, v198
	v_mul_f32_e32 v199, 0x43000000, v199
	ds_write2_b32 v210, v198, v199 offset0:172 offset1:238
	v_mul_f32_e32 v200, 0x43000000, v200
	v_mul_f32_e32 v201, 0x43000000, v201
	ds_write2_b32 v211, v200, v201 offset0:48 offset1:114
	v_mul_f32_e32 v202, 0x43000000, v202
	v_mul_f32_e32 v203, 0x43000000, v203
	ds_write2_b32 v211, v202, v203 offset0:180 offset1:246
	v_mul_f32_e32 v204, 0x43000000, v204
	v_mul_f32_e32 v205, 0x43000000, v205
	ds_write2_b32 v212, v204, v205 offset0:56 offset1:122
	v_mul_f32_e32 v206, 0x43000000, v206
	v_mul_f32_e32 v207, 0x43000000, v207
	ds_write2_b32 v212, v206, v207 offset0:188 offset1:254
	s_waitcnt lgkmcnt(0)
	ds_read2_b32 v[214:215], v21 offset1:8
	ds_read2_b32 v[216:217], v21 offset0:33 offset1:41
	ds_read2_b32 v[218:219], v21 offset0:66 offset1:74
	ds_read2_b32 v[220:221], v21 offset0:99 offset1:107
	ds_read2_b32 v[222:223], v21 offset0:132 offset1:140
	ds_read2_b32 v[224:225], v21 offset0:165 offset1:173
	ds_read2_b32 v[226:227], v21 offset0:198 offset1:206
	ds_read2_b32 v[228:229], v21 offset0:231 offset1:239
	s_waitcnt lgkmcnt(0)
	v_max_f32_e32 v214, v214, v214
	v_max_f32_e32 v216, v216, v216
	v_max_f32_e32 v218, v218, v218
	v_max_f32_e32 v220, v220, v220
	v_max_f32_e32 v222, v222, v222
	v_max_f32_e32 v224, v224, v224
	v_max_f32_e32 v226, v226, v226
	v_max_f32_e32 v228, v228, v228
	v_med3_f32 v214, v214, s44, v64
	v_med3_f32 v216, v216, s44, v64
	v_med3_f32 v218, v218, s44, v64
	v_med3_f32 v220, v220, s44, v64
	v_med3_f32 v222, v222, s44, v64
	v_med3_f32 v224, v224, s44, v64
	v_med3_f32 v226, v226, s44, v64
	v_med3_f32 v228, v228, s44, v64
	v_mov_b32_e32 v230, v11
	v_mov_b32_e32 v231, v11
	v_or_b32_e32 v233, s36, v20
	v_cvt_pk_fp8_f32 v230, v214, v216
	v_cvt_pk_fp8_f32 v231, v222, v224
	v_lshl_add_u32 v232, v233, 14, v8
	v_cvt_pk_fp8_f32 v230, v218, v220 op_sel:[0,0,1]
	v_cvt_pk_fp8_f32 v231, v226, v228 op_sel:[0,0,1]
	s_nop 0
	global_store_dwordx2 v232, v[230:231], s[20:21]
	s_nop 1
	v_max_f32_e32 v215, v215, v215
	v_max_f32_e32 v217, v217, v217
	v_max_f32_e32 v219, v219, v219
	v_max_f32_e32 v221, v221, v221
	v_max_f32_e32 v223, v223, v223
	v_max_f32_e32 v225, v225, v225
	v_max_f32_e32 v227, v227, v227
	v_max_f32_e32 v229, v229, v229
	v_med3_f32 v215, v215, s44, v64
	v_med3_f32 v217, v217, s44, v64
	v_med3_f32 v219, v219, s44, v64
	v_med3_f32 v221, v221, s44, v64
	v_med3_f32 v223, v223, s44, v64
	v_med3_f32 v225, v225, s44, v64
	v_med3_f32 v227, v227, s44, v64
	v_med3_f32 v229, v229, s44, v64
	v_mov_b32_e32 v230, v11
	v_mov_b32_e32 v231, v11
	v_or_b32_e32 v233, s36, v22
	v_cvt_pk_fp8_f32 v230, v215, v217
	v_cvt_pk_fp8_f32 v231, v223, v225
	v_lshl_add_u32 v232, v233, 14, v8
	v_cvt_pk_fp8_f32 v230, v219, v221 op_sel:[0,0,1]
	v_cvt_pk_fp8_f32 v231, v227, v229 op_sel:[0,0,1]
	s_nop 0
	global_store_dwordx2 v232, v[230:231], s[20:21]
	s_nop 1
	ds_read2_b32 v[214:215], v21 offset0:16 offset1:24
	ds_read2_b32 v[216:217], v21 offset0:49 offset1:57
	ds_read2_b32 v[218:219], v21 offset0:82 offset1:90
	ds_read2_b32 v[220:221], v21 offset0:115 offset1:123
	ds_read2_b32 v[222:223], v21 offset0:148 offset1:156
	ds_read2_b32 v[224:225], v21 offset0:181 offset1:189
	ds_read2_b32 v[226:227], v21 offset0:214 offset1:222
	ds_read2_b32 v[228:229], v21 offset0:247 offset1:255
	s_waitcnt lgkmcnt(0)
	v_max_f32_e32 v214, v214, v214
	v_max_f32_e32 v216, v216, v216
	v_max_f32_e32 v218, v218, v218
	v_max_f32_e32 v220, v220, v220
	v_max_f32_e32 v222, v222, v222
	v_max_f32_e32 v224, v224, v224
	v_max_f32_e32 v226, v226, v226
	v_max_f32_e32 v228, v228, v228
	v_med3_f32 v214, v214, s44, v64
	v_med3_f32 v216, v216, s44, v64
	v_med3_f32 v218, v218, s44, v64
	v_med3_f32 v220, v220, s44, v64
	v_med3_f32 v222, v222, s44, v64
	v_med3_f32 v224, v224, s44, v64
	v_med3_f32 v226, v226, s44, v64
	v_med3_f32 v228, v228, s44, v64
	v_mov_b32_e32 v230, v11
	v_mov_b32_e32 v231, v11
	v_or_b32_e32 v233, s36, v23
	v_cvt_pk_fp8_f32 v230, v214, v216
	v_cvt_pk_fp8_f32 v231, v222, v224
	v_lshl_add_u32 v232, v233, 14, v8
	v_cvt_pk_fp8_f32 v230, v218, v220 op_sel:[0,0,1]
	v_cvt_pk_fp8_f32 v231, v226, v228 op_sel:[0,0,1]
	s_nop 0
	global_store_dwordx2 v232, v[230:231], s[20:21]
	s_nop 1
	v_max_f32_e32 v215, v215, v215
	v_max_f32_e32 v217, v217, v217
	v_max_f32_e32 v219, v219, v219
	v_max_f32_e32 v221, v221, v221
	v_max_f32_e32 v223, v223, v223
	v_max_f32_e32 v225, v225, v225
	v_max_f32_e32 v227, v227, v227
	v_max_f32_e32 v229, v229, v229
	v_med3_f32 v215, v215, s44, v64
	v_med3_f32 v217, v217, s44, v64
	v_med3_f32 v219, v219, s44, v64
	v_med3_f32 v221, v221, s44, v64
	v_med3_f32 v223, v223, s44, v64
	v_med3_f32 v225, v225, s44, v64
	v_med3_f32 v227, v227, s44, v64
	v_med3_f32 v229, v229, s44, v64
	v_mov_b32_e32 v230, v11
	v_mov_b32_e32 v231, v11
	v_or_b32_e32 v233, s36, v24
	v_cvt_pk_fp8_f32 v230, v215, v217
	v_cvt_pk_fp8_f32 v231, v223, v225
	v_lshl_add_u32 v232, v233, 14, v8
	v_cvt_pk_fp8_f32 v230, v219, v221 op_sel:[0,0,1]
	v_cvt_pk_fp8_f32 v231, v227, v229 op_sel:[0,0,1]
	s_nop 0
	global_store_dwordx2 v232, v[230:231], s[20:21]
	s_nop 1
	s_waitcnt lgkmcnt(0)
	s_add_i32 s50, s50, s96
	s_add_i32 s39, s39, s76
	s_add_i32 s40, s40, s41
	s_add_i32 s42, s42, s43
	s_add_i32 s51, s51, s96
	s_branch .Lwd_orig
; #define GAS __attribute__((address_space(1)))
; #define LAS __attribute__((address_space(3)))
;     const int pr = item >> 1, kb = 2 * (pr / nblk) + (item & 1), nb = pr % nblk, k0 = 64 * kb, n0 = 32 * nb;
;     const int nr = n0 + (lane & 31); const int sc = MAP == 1 ? src_col_in(nr) : nr;
;     float v[32];
; #pragma unroll
;     for (int i = 0; i < 32; ++i) v[i] = sc >= 0 ? W[(size_t)(k0 + 2 * i + (lane >> 5)) * Nsrc + sc] : 0.f;
; #pragma unroll
;     for (int i = 0; i < 32; ++i) { const int k = k0 + 2 * i + (lane >> 5); float x = v[i] * wscale; if (KS) x *= (k < ksplit ? ksA[k] : ksB[k - ksplit]); scr[(2 * i + (lane >> 5)) * 33 + (lane & 31)] = x; }
;     LDS_WAIT(); asm volatile("" ::: "memory");
;     const int c = lane & 7;
; #pragma unroll
;     for (int j = 0; j < 4; ++j) { const int n = (lane >> 3) + 8 * j; const LAS float* s = scr + (8 * c) * 33 + n;
;         const unsigned long long o = (unsigned long long)pg8::pk4_fp8(s[0 * 33], s[1 * 33], s[2 * 33], s[3 * 33]) | ((unsigned long long)pg8::pk4_fp8(s[4 * 33], s[5 * 33], s[6 * 33], s[7 * 33]) << 32);
;         *(GAS unsigned long long*)(WT + (size_t)(n0 + n) * K + k0 + 8 * c) = o; }
;     LDS_WAIT(); asm volatile("" ::: "memory");
; }
; __global__ void __launch_bounds__(NWAVES * 64, 2) hybrid_fwd(Args args) {
;     ...
;         for (int it = gw; it < DEPTH * I_L; it += NGW) {
;             const int l = it / I_L; int r = it % I_L;
;             if (r < I_IN) { if (l >= PROJ_F8_FROM) p0_transpose_item_f8<true, 1>(args.in[2] + (size_t)l * DM * NSRC, DM, NSRC, NPROJ / 32, (unsigned char*)(ws + WS_WIN + l * SZ_WIN), WUP8_SCALE, args.in[1] + l * DM, args.in[1] + l * DM, DM, scr, r, lane);
;                 else p0_transpose_item<1, true>(args.in[2] + (size_t)l * DM * NSRC, DM, NSRC, NPROJ / 32, (bf16*)(ws + WS_WIN + l * SZ_WIN), args.in[1] + l * DM, args.in[1] + l * DM, DM, scr, r, lane); continue; } r -= I_IN;
;             if (r < I_O) { if (l >= WO_F8_FROM) p0_transpose_item_f8<true>(args.in[13] + (size_t)l * DM * DM, DM, DM, DM / 32, (unsigned char*)(ws + WS_WO + l * SZ_WO), 64.f, args.in[6] + l * 2048, args.in[12] + l * 2048, 2048, scr, r, lane);
;                 else p0_transpose_item<0, true>(args.in[13] + (size_t)l * DM * DM, DM, DM, DM / 32, (bf16*)(ws + WS_WO + l * SZ_WO), args.in[6] + l * 2048, args.in[12] + l * 2048, 2048, scr, r, lane); continue; } r -= I_O;
.Lwd_loopY_more:
	s_add_i32 s50, s50, s96
	s_add_i32 s39, s39, s76
	s_add_i32 s40, s40, s41
	s_add_i32 s42, s42, s43
	s_add_i32 s51, s51, s96
	s_add_i32 s20, s51, 0xffff0600
	s_lshr_b32 s4, s20, 7
	s_and_b32 s4, s4, 0xfe
	s_and_b32 s5, s20, 1
	s_or_b32 s4, s4, s5
	s_lshl_b32 s4, s4, 6
	s_lshl_b32 s5, s20, 4
	s_and_b32 s5, s5, 0xfe0
	s_waitcnt vmcnt(31)
	v_or_b32_e32 v208, s4, v6
	v_lshlrev_b32_e32 v208, 12, v208
	v_or3_b32 v208, s5, v18, v208
	v_lshlrev_b32_e32 v208, 2, v208
	s_mov_b64 s[8:9], s[10:11]
	global_load_dword v144, v208, s[8:9]
	s_add_u32 s8, s8, 0x8000
	s_addc_u32 s9, s9, 0
	global_load_dword v145, v208, s[8:9]
	s_add_u32 s8, s8, 0x8000
	s_addc_u32 s9, s9, 0
	global_load_dword v146, v208, s[8:9]
	s_add_u32 s8, s8, 0x8000
	s_addc_u32 s9, s9, 0
	global_load_dword v147, v208, s[8:9]
	s_add_u32 s8, s8, 0x8000
	s_addc_u32 s9, s9, 0
	global_load_dword v148, v208, s[8:9]
	s_add_u32 s8, s8, 0x8000
	s_addc_u32 s9, s9, 0
	global_load_dword v149, v208, s[8:9]
	s_add_u32 s8, s8, 0x8000
	s_addc_u32 s9, s9, 0
	global_load_dword v150, v208, s[8:9]
	s_add_u32 s8, s8, 0x8000
	s_addc_u32 s9, s9, 0
	global_load_dword v151, v208, s[8:9]
	s_add_u32 s8, s8, 0x8000
	s_addc_u32 s9, s9, 0
	global_load_dword v152, v208, s[8:9]
	s_add_u32 s8, s8, 0x8000
	s_addc_u32 s9, s9, 0
	global_load_dword v153, v208, s[8:9]
	s_add_u32 s8, s8, 0x8000
	s_addc_u32 s9, s9, 0
	global_load_dword v154, v208, s[8:9]
	s_add_u32 s8, s8, 0x8000
	s_addc_u32 s9, s9, 0
	global_load_dword v155, v208, s[8:9]
	s_add_u32 s8, s8, 0x8000
	s_addc_u32 s9, s9, 0
	global_load_dword v156, v208, s[8:9]
	s_add_u32 s8, s8, 0x8000
	s_addc_u32 s9, s9, 0
	global_load_dword v157, v208, s[8:9]
	s_add_u32 s8, s8, 0x8000
	s_addc_u32 s9, s9, 0
	global_load_dword v158, v208, s[8:9]
	s_add_u32 s8, s8, 0x8000
	s_addc_u32 s9, s9, 0
	global_load_dword v159, v208, s[8:9]
	s_add_u32 s8, s8, 0x8000
	s_addc_u32 s9, s9, 0
	global_load_dword v160, v208, s[8:9]
	s_add_u32 s8, s8, 0x8000
	s_addc_u32 s9, s9, 0
	global_load_dword v161, v208, s[8:9]
	s_add_u32 s8, s8, 0x8000
	s_addc_u32 s9, s9, 0
	global_load_dword v162, v208, s[8:9]
	s_add_u32 s8, s8, 0x8000
	s_addc_u32 s9, s9, 0
	global_load_dword v163, v208, s[8:9]
	s_add_u32 s8, s8, 0x8000
	s_addc_u32 s9, s9, 0
	global_load_dword v164, v208, s[8:9]
	s_add_u32 s8, s8, 0x8000
	s_addc_u32 s9, s9, 0
	global_load_dword v165, v208, s[8:9]
	s_add_u32 s8, s8, 0x8000
	s_addc_u32 s9, s9, 0
	global_load_dword v166, v208, s[8:9]
	s_add_u32 s8, s8, 0x8000
	s_addc_u32 s9, s9, 0
	global_load_dword v167, v208, s[8:9]
	s_add_u32 s8, s8, 0x8000
	s_addc_u32 s9, s9, 0
	global_load_dword v168, v208, s[8:9]
	s_add_u32 s8, s8, 0x8000
	s_addc_u32 s9, s9, 0
	global_load_dword v169, v208, s[8:9]
	s_add_u32 s8, s8, 0x8000
	s_addc_u32 s9, s9, 0
	global_load_dword v170, v208, s[8:9]
	s_add_u32 s8, s8, 0x8000
	s_addc_u32 s9, s9, 0
	global_load_dword v171, v208, s[8:9]
	s_add_u32 s8, s8, 0x8000
	s_addc_u32 s9, s9, 0
	global_load_dword v172, v208, s[8:9]
	s_add_u32 s8, s8, 0x8000
	s_addc_u32 s9, s9, 0
	global_load_dword v173, v208, s[8:9]
	s_add_u32 s8, s8, 0x8000
	s_addc_u32 s9, s9, 0
	global_load_dword v174, v208, s[8:9]
	s_add_u32 s8, s8, 0x8000
	s_addc_u32 s9, s9, 0
	global_load_dword v175, v208, s[8:9]
	s_waitcnt vmcnt(36)
	s_add_u32 s20, s30, s16
	s_addc_u32 s21, s31, 0
	v_add_u32_e32 v209, 0x1000, v19
	v_add_u32_e32 v210, 0x1400, v19
	v_add_u32_e32 v211, 0x1800, v19
	v_add_u32_e32 v212, 0x1c00, v19
	v_mul_f32_e32 v176, 0x43000000, v176
	v_mul_f32_e32 v177, 0x43000000, v177
	ds_write2_b32 v19, v176, v177 offset1:66
	v_mul_f32_e32 v178, 0x43000000, v178
	v_mul_f32_e32 v179, 0x43000000, v179
	ds_write2_b32 v19, v178, v179 offset0:132 offset1:198
	v_mul_f32_e32 v180, 0x43000000, v180
	v_mul_f32_e32 v181, 0x43000000, v181
	ds_write2_b32 v61, v180, v181 offset0:8 offset1:74
	v_mul_f32_e32 v182, 0x43000000, v182
	v_mul_f32_e32 v183, 0x43000000, v183
	ds_write2_b32 v61, v182, v183 offset0:140 offset1:206
	v_mul_f32_e32 v184, 0x43000000, v184
	v_mul_f32_e32 v185, 0x43000000, v185
	ds_write2_b32 v62, v184, v185 offset0:16 offset1:82
	v_mul_f32_e32 v186, 0x43000000, v186
	v_mul_f32_e32 v187, 0x43000000, v187
	ds_write2_b32 v62, v186, v187 offset0:148 offset1:214
	v_mul_f32_e32 v188, 0x43000000, v188
	v_mul_f32_e32 v189, 0x43000000, v189
	ds_write2_b32 v63, v188, v189 offset0:24 offset1:90
	v_mul_f32_e32 v190, 0x43000000, v190
	v_mul_f32_e32 v191, 0x43000000, v191
	ds_write2_b32 v63, v190, v191 offset0:156 offset1:222
	v_mul_f32_e32 v192, 0x43000000, v192
	v_mul_f32_e32 v193, 0x43000000, v193
	ds_write2_b32 v209, v192, v193 offset0:32 offset1:98
	v_mul_f32_e32 v194, 0x43000000, v194
	v_mul_f32_e32 v195, 0x43000000, v195
	ds_write2_b32 v209, v194, v195 offset0:164 offset1:230
	v_mul_f32_e32 v196, 0x43000000, v196
	v_mul_f32_e32 v197, 0x43000000, v197
	ds_write2_b32 v210, v196, v197 offset0:40 offset1:106
	v_mul_f32_e32 v198, 0x43000000, v198
	v_mul_f32_e32 v199, 0x43000000, v199
	ds_write2_b32 v210, v198, v199 offset0:172 offset1:238
	v_mul_f32_e32 v200, 0x43000000, v200
	v_mul_f32_e32 v201, 0x43000000, v201
	ds_write2_b32 v211, v200, v201 offset0:48 offset1:114
	v_mul_f32_e32 v202, 0x43000000, v202
	v_mul_f32_e32 v203, 0x43000000, v203
	ds_write2_b32 v211, v202, v203 offset0:180 offset1:246
	v_mul_f32_e32 v204, 0x43000000, v204
	v_mul_f32_e32 v205, 0x43000000, v205
	ds_write2_b32 v212, v204, v205 offset0:56 offset1:122
	v_mul_f32_e32 v206, 0x43000000, v206
	v_mul_f32_e32 v207, 0x43000000, v207
	ds_write2_b32 v212, v206, v207 offset0:188 offset1:254
	s_waitcnt lgkmcnt(0)
; #define GAS __attribute__((address_space(1)))
; #define LAS __attribute__((address_space(3)))
; #define LDS_WAIT() asm volatile("s_waitcnt lgkmcnt(0)" ::: "memory")
;     const int pr = item >> 1, kb = 2 * (pr / nblk) + (item & 1), nb = pr % nblk, k0 = 64 * kb, n0 = 32 * nb;
;     const int nr = n0 + (lane & 31); const int sc = MAP == 1 ? src_col_in(nr) : nr;
;     float v[32];
; #pragma unroll
;     for (int i = 0; i < 32; ++i) v[i] = sc >= 0 ? W[(size_t)(k0 + 2 * i + (lane >> 5)) * Nsrc + sc] : 0.f;
; #pragma unroll
;     for (int i = 0; i < 32; ++i) { const int k = k0 + 2 * i + (lane >> 5); float x = v[i] * wscale; if (KS) x *= (k < ksplit ? ksA[k] : ksB[k - ksplit]); scr[(2 * i + (lane >> 5)) * 33 + (lane & 31)] = x; }
;     LDS_WAIT(); asm volatile("" ::: "memory");
;     const int c = lane & 7;
; #pragma unroll
;     for (int j = 0; j < 4; ++j) { const int n = (lane >> 3) + 8 * j; const LAS float* s = scr + (8 * c) * 33 + n;
;         const unsigned long long o = (unsigned long long)pg8::pk4_fp8(s[0 * 33], s[1 * 33], s[2 * 33], s[3 * 33]) | ((unsigned long long)pg8::pk4_fp8(s[4 * 33], s[5 * 33], s[6 * 33], s[7 * 33]) << 32);
;         *(GAS unsigned long long*)(WT + (size_t)(n0 + n) * K + k0 + 8 * c) = o; }
;     LDS_WAIT(); asm volatile("" ::: "memory");
; }
	ds_read2_b32 v[214:215], v21 offset1:8
	ds_read2_b32 v[216:217], v21 offset0:33 offset1:41
	ds_read2_b32 v[218:219], v21 offset0:66 offset1:74
	ds_read2_b32 v[220:221], v21 offset0:99 offset1:107
	ds_read2_b32 v[222:223], v21 offset0:132 offset1:140
	ds_read2_b32 v[224:225], v21 offset0:165 offset1:173
	ds_read2_b32 v[226:227], v21 offset0:198 offset1:206
	ds_read2_b32 v[228:229], v21 offset0:231 offset1:239
	s_waitcnt lgkmcnt(0)
	v_max_f32_e32 v214, v214, v214
	v_max_f32_e32 v216, v216, v216
	v_max_f32_e32 v218, v218, v218
	v_max_f32_e32 v220, v220, v220
	v_max_f32_e32 v222, v222, v222
	v_max_f32_e32 v224, v224, v224
	v_max_f32_e32 v226, v226, v226
	v_max_f32_e32 v228, v228, v228
	v_med3_f32 v214, v214, s44, v64
	v_med3_f32 v216, v216, s44, v64
	v_med3_f32 v218, v218, s44, v64
	v_med3_f32 v220, v220, s44, v64
	v_med3_f32 v222, v222, s44, v64
	v_med3_f32 v224, v224, s44, v64
	v_med3_f32 v226, v226, s44, v64
	v_med3_f32 v228, v228, s44, v64
	v_mov_b32_e32 v230, v11
	v_mov_b32_e32 v231, v11
	v_or_b32_e32 v233, s36, v20
	v_cvt_pk_fp8_f32 v230, v214, v216
	v_cvt_pk_fp8_f32 v231, v222, v224
	v_lshl_add_u32 v232, v233, 14, v8
	v_cvt_pk_fp8_f32 v230, v218, v220 op_sel:[0,0,1]
	v_cvt_pk_fp8_f32 v231, v226, v228 op_sel:[0,0,1]
	s_nop 0
	global_store_dwordx2 v232, v[230:231], s[20:21]
	s_nop 1
	v_max_f32_e32 v215, v215, v215
	v_max_f32_e32 v217, v217, v217
	v_max_f32_e32 v219, v219, v219
	v_max_f32_e32 v221, v221, v221
	v_max_f32_e32 v223, v223, v223
	v_max_f32_e32 v225, v225, v225
	v_max_f32_e32 v227, v227, v227
	v_max_f32_e32 v229, v229, v229
	v_med3_f32 v215, v215, s44, v64
	v_med3_f32 v217, v217, s44, v64
	v_med3_f32 v219, v219, s44, v64
	v_med3_f32 v221, v221, s44, v64
	v_med3_f32 v223, v223, s44, v64
	v_med3_f32 v225, v225, s44, v64
	v_med3_f32 v227, v227, s44, v64
	v_med3_f32 v229, v229, s44, v64
	v_mov_b32_e32 v230, v11
	v_mov_b32_e32 v231, v11
	v_or_b32_e32 v233, s36, v22
	v_cvt_pk_fp8_f32 v230, v215, v217
	v_cvt_pk_fp8_f32 v231, v223, v225
	v_lshl_add_u32 v232, v233, 14, v8
	v_cvt_pk_fp8_f32 v230, v219, v221 op_sel:[0,0,1]
	v_cvt_pk_fp8_f32 v231, v227, v229 op_sel:[0,0,1]
	s_nop 0
	global_store_dwordx2 v232, v[230:231], s[20:21]
	s_nop 1
	ds_read2_b32 v[214:215], v21 offset0:16 offset1:24
	ds_read2_b32 v[216:217], v21 offset0:49 offset1:57
	ds_read2_b32 v[218:219], v21 offset0:82 offset1:90
	ds_read2_b32 v[220:221], v21 offset0:115 offset1:123
	ds_read2_b32 v[222:223], v21 offset0:148 offset1:156
	ds_read2_b32 v[224:225], v21 offset0:181 offset1:189
	ds_read2_b32 v[226:227], v21 offset0:214 offset1:222
	ds_read2_b32 v[228:229], v21 offset0:247 offset1:255
	s_waitcnt lgkmcnt(0)
	v_max_f32_e32 v214, v214, v214
	v_max_f32_e32 v216, v216, v216
	v_max_f32_e32 v218, v218, v218
	v_max_f32_e32 v220, v220, v220
	v_max_f32_e32 v222, v222, v222
	v_max_f32_e32 v224, v224, v224
	v_max_f32_e32 v226, v226, v226
	v_max_f32_e32 v228, v228, v228
	v_med3_f32 v214, v214, s44, v64
	v_med3_f32 v216, v216, s44, v64
	v_med3_f32 v218, v218, s44, v64
	v_med3_f32 v220, v220, s44, v64
	v_med3_f32 v222, v222, s44, v64
	v_med3_f32 v224, v224, s44, v64
	v_med3_f32 v226, v226, s44, v64
	v_med3_f32 v228, v228, s44, v64
	v_mov_b32_e32 v230, v11
	v_mov_b32_e32 v231, v11
	v_or_b32_e32 v233, s36, v23
	v_cvt_pk_fp8_f32 v230, v214, v216
	v_cvt_pk_fp8_f32 v231, v222, v224
	v_lshl_add_u32 v232, v233, 14, v8
	v_cvt_pk_fp8_f32 v230, v218, v220 op_sel:[0,0,1]
	v_cvt_pk_fp8_f32 v231, v226, v228 op_sel:[0,0,1]
	s_nop 0
	global_store_dwordx2 v232, v[230:231], s[20:21]
	s_nop 1
	v_max_f32_e32 v215, v215, v215
	v_max_f32_e32 v217, v217, v217
	v_max_f32_e32 v219, v219, v219
	v_max_f32_e32 v221, v221, v221
	v_max_f32_e32 v223, v223, v223
	v_max_f32_e32 v225, v225, v225
	v_max_f32_e32 v227, v227, v227
	v_max_f32_e32 v229, v229, v229
	v_med3_f32 v215, v215, s44, v64
	v_med3_f32 v217, v217, s44, v64
	v_med3_f32 v219, v219, s44, v64
	v_med3_f32 v221, v221, s44, v64
	v_med3_f32 v223, v223, s44, v64
	v_med3_f32 v225, v225, s44, v64
	v_med3_f32 v227, v227, s44, v64
	v_med3_f32 v229, v229, s44, v64
	v_mov_b32_e32 v230, v11
	v_mov_b32_e32 v231, v11
	v_or_b32_e32 v233, s36, v24
	v_cvt_pk_fp8_f32 v230, v215, v217
	v_cvt_pk_fp8_f32 v231, v223, v225
	v_lshl_add_u32 v232, v233, 14, v8
	v_cvt_pk_fp8_f32 v230, v219, v221 op_sel:[0,0,1]
	v_cvt_pk_fp8_f32 v231, v227, v229 op_sel:[0,0,1]
	s_nop 0
	global_store_dwordx2 v232, v[230:231], s[20:21]
	s_nop 1
	s_waitcnt lgkmcnt(0)
	s_mov_b32 s16, s4
	s_mov_b32 s36, s5
; #define GAS __attribute__((address_space(1)))
; #define LAS __attribute__((address_space(3)))
;     const int pr = item >> 1, kb = 2 * (pr / nblk) + (item & 1), nb = pr % nblk, k0 = 64 * kb, n0 = 32 * nb;
;     const int nr = n0 + (lane & 31); const int sc = MAP == 1 ? src_col_in(nr) : nr;
;     float v[32];
; #pragma unroll
;     for (int i = 0; i < 32; ++i) v[i] = sc >= 0 ? W[(size_t)(k0 + 2 * i + (lane >> 5)) * Nsrc + sc] : 0.f;
; #pragma unroll
;     for (int i = 0; i < 32; ++i) { const int k = k0 + 2 * i + (lane >> 5); float x = v[i] * wscale; if (KS) x *= (k < ksplit ? ksA[k] : ksB[k - ksplit]); scr[(2 * i + (lane >> 5)) * 33 + (lane & 31)] = x; }
;     LDS_WAIT(); asm volatile("" ::: "memory");
;     const int c = lane & 7;
; #pragma unroll
;     for (int j = 0; j < 4; ++j) { const int n = (lane >> 3) + 8 * j; const LAS float* s = scr + (8 * c) * 33 + n;
;         const unsigned long long o = (unsigned long long)pg8::pk4_fp8(s[0 * 33], s[1 * 33], s[2 * 33], s[3 * 33]) | ((unsigned long long)pg8::pk4_fp8(s[4 * 33], s[5 * 33], s[6 * 33], s[7 * 33]) << 32);
;         *(GAS unsigned long long*)(WT + (size_t)(n0 + n) * K + k0 + 8 * c) = o; }
;     LDS_WAIT(); asm volatile("" ::: "memory");
; }
; __global__ void __launch_bounds__(NWAVES * 64, 2) hybrid_fwd(Args args) {
;     ...
;         for (int it = gw; it < DEPTH * I_L; it += NGW) {
;             const int l = it / I_L; int r = it % I_L;
;             if (r < I_IN) { if (l >= PROJ_F8_FROM) p0_transpose_item_f8<true, 1>(args.in[2] + (size_t)l * DM * NSRC, DM, NSRC, NPROJ / 32, (unsigned char*)(ws + WS_WIN + l * SZ_WIN), WUP8_SCALE, args.in[1] + l * DM, args.in[1] + l * DM, DM, scr, r, lane);
;                 else p0_transpose_item<1, true>(args.in[2] + (size_t)l * DM * NSRC, DM, NSRC, NPROJ / 32, (bf16*)(ws + WS_WIN + l * SZ_WIN), args.in[1] + l * DM, args.in[1] + l * DM, DM, scr, r, lane); continue; } r -= I_IN;
;             if (r < I_O) { if (l >= WO_F8_FROM) p0_transpose_item_f8<true>(args.in[13] + (size_t)l * DM * DM, DM, DM, DM / 32, (unsigned char*)(ws + WS_WO + l * SZ_WO), 64.f, args.in[6] + l * 2048, args.in[12] + l * 2048, 2048, scr, r, lane);
;                 else p0_transpose_item<0, true>(args.in[13] + (size_t)l * DM * DM, DM, DM, DM / 32, (bf16*)(ws + WS_WO + l * SZ_WO), args.in[6] + l * 2048, args.in[12] + l * 2048, 2048, scr, r, lane); continue; } r -= I_O;
.Lwd_loopX:
	s_add_i32 s4, s51, s96
	s_add_i32 s4, s4, s96
	s_cmp_gt_i32 s4, 0x179ff
	s_cbranch_scc0 .Lwd_loopX_more
	s_waitcnt vmcnt(4)
	s_add_u32 s20, s30, s16
	s_addc_u32 s21, s31, 0
	v_add_u32_e32 v209, 0x1000, v19
	v_add_u32_e32 v210, 0x1400, v19
	v_add_u32_e32 v211, 0x1800, v19
	v_add_u32_e32 v212, 0x1c00, v19
	v_mul_f32_e32 v144, 0x43000000, v144
	v_mul_f32_e32 v145, 0x43000000, v145
	ds_write2_b32 v19, v144, v145 offset1:66
	v_mul_f32_e32 v146, 0x43000000, v146
	v_mul_f32_e32 v147, 0x43000000, v147
	ds_write2_b32 v19, v146, v147 offset0:132 offset1:198
	v_mul_f32_e32 v148, 0x43000000, v148
	v_mul_f32_e32 v149, 0x43000000, v149
	ds_write2_b32 v61, v148, v149 offset0:8 offset1:74
	v_mul_f32_e32 v150, 0x43000000, v150
	v_mul_f32_e32 v151, 0x43000000, v151
	ds_write2_b32 v61, v150, v151 offset0:140 offset1:206
	v_mul_f32_e32 v152, 0x43000000, v152
	v_mul_f32_e32 v153, 0x43000000, v153
	ds_write2_b32 v62, v152, v153 offset0:16 offset1:82
	v_mul_f32_e32 v154, 0x43000000, v154
	v_mul_f32_e32 v155, 0x43000000, v155
	ds_write2_b32 v62, v154, v155 offset0:148 offset1:214
	v_mul_f32_e32 v156, 0x43000000, v156
	v_mul_f32_e32 v157, 0x43000000, v157
	ds_write2_b32 v63, v156, v157 offset0:24 offset1:90
	v_mul_f32_e32 v158, 0x43000000, v158
	v_mul_f32_e32 v159, 0x43000000, v159
	ds_write2_b32 v63, v158, v159 offset0:156 offset1:222
	v_mul_f32_e32 v160, 0x43000000, v160
	v_mul_f32_e32 v161, 0x43000000, v161
	ds_write2_b32 v209, v160, v161 offset0:32 offset1:98
	v_mul_f32_e32 v162, 0x43000000, v162
	v_mul_f32_e32 v163, 0x43000000, v163
	ds_write2_b32 v209, v162, v163 offset0:164 offset1:230
	v_mul_f32_e32 v164, 0x43000000, v164
	v_mul_f32_e32 v165, 0x43000000, v165
	ds_write2_b32 v210, v164, v165 offset0:40 offset1:106
	v_mul_f32_e32 v166, 0x43000000, v166
	v_mul_f32_e32 v167, 0x43000000, v167
	ds_write2_b32 v210, v166, v167 offset0:172 offset1:238
	v_mul_f32_e32 v168, 0x43000000, v168
	v_mul_f32_e32 v169, 0x43000000, v169
	ds_write2_b32 v211, v168, v169 offset0:48 offset1:114
	v_mul_f32_e32 v170, 0x43000000, v170
	v_mul_f32_e32 v171, 0x43000000, v171
	ds_write2_b32 v211, v170, v171 offset0:180 offset1:246
	v_mul_f32_e32 v172, 0x43000000, v172
	v_mul_f32_e32 v173, 0x43000000, v173
	ds_write2_b32 v212, v172, v173 offset0:56 offset1:122
	v_mul_f32_e32 v174, 0x43000000, v174
	v_mul_f32_e32 v175, 0x43000000, v175
	ds_write2_b32 v212, v174, v175 offset0:188 offset1:254
	s_waitcnt lgkmcnt(0)
	ds_read2_b32 v[214:215], v21 offset1:8
	ds_read2_b32 v[216:217], v21 offset0:33 offset1:41
	ds_read2_b32 v[218:219], v21 offset0:66 offset1:74
	ds_read2_b32 v[220:221], v21 offset0:99 offset1:107
	ds_read2_b32 v[222:223], v21 offset0:132 offset1:140
	ds_read2_b32 v[224:225], v21 offset0:165 offset1:173
	ds_read2_b32 v[226:227], v21 offset0:198 offset1:206
	ds_read2_b32 v[228:229], v21 offset0:231 offset1:239
	s_waitcnt lgkmcnt(0)
	v_max_f32_e32 v214, v214, v214
	v_max_f32_e32 v216, v216, v216
	v_max_f32_e32 v218, v218, v218
	v_max_f32_e32 v220, v220, v220
	v_max_f32_e32 v222, v222, v222
	v_max_f32_e32 v224, v224, v224
	v_max_f32_e32 v226, v226, v226
	v_max_f32_e32 v228, v228, v228
	v_med3_f32 v214, v214, s44, v64
	v_med3_f32 v216, v216, s44, v64
	v_med3_f32 v218, v218, s44, v64
	v_med3_f32 v220, v220, s44, v64
	v_med3_f32 v222, v222, s44, v64
	v_med3_f32 v224, v224, s44, v64
	v_med3_f32 v226, v226, s44, v64
	v_med3_f32 v228, v228, s44, v64
	v_mov_b32_e32 v230, v11
	v_mov_b32_e32 v231, v11
	v_or_b32_e32 v233, s36, v20
	v_cvt_pk_fp8_f32 v230, v214, v216
	v_cvt_pk_fp8_f32 v231, v222, v224
	v_lshl_add_u32 v232, v233, 14, v8
	v_cvt_pk_fp8_f32 v230, v218, v220 op_sel:[0,0,1]
	v_cvt_pk_fp8_f32 v231, v226, v228 op_sel:[0,0,1]
	s_nop 0
	global_store_dwordx2 v232, v[230:231], s[20:21]
	s_nop 1
	v_max_f32_e32 v215, v215, v215
	v_max_f32_e32 v217, v217, v217
	v_max_f32_e32 v219, v219, v219
	v_max_f32_e32 v221, v221, v221
	v_max_f32_e32 v223, v223, v223
	v_max_f32_e32 v225, v225, v225
	v_max_f32_e32 v227, v227, v227
	v_max_f32_e32 v229, v229, v229
	v_med3_f32 v215, v215, s44, v64
	v_med3_f32 v217, v217, s44, v64
	v_med3_f32 v219, v219, s44, v64
	v_med3_f32 v221, v221, s44, v64
	v_med3_f32 v223, v223, s44, v64
	v_med3_f32 v225, v225, s44, v64
	v_med3_f32 v227, v227, s44, v64
	v_med3_f32 v229, v229, s44, v64
	v_mov_b32_e32 v230, v11
	v_mov_b32_e32 v231, v11
	v_or_b32_e32 v233, s36, v22
	v_cvt_pk_fp8_f32 v230, v215, v217
	v_cvt_pk_fp8_f32 v231, v223, v225
	v_lshl_add_u32 v232, v233, 14, v8
	v_cvt_pk_fp8_f32 v230, v219, v221 op_sel:[0,0,1]
	v_cvt_pk_fp8_f32 v231, v227, v229 op_sel:[0,0,1]
	s_nop 0
	global_store_dwordx2 v232, v[230:231], s[20:21]
	s_nop 1
	ds_read2_b32 v[214:215], v21 offset0:16 offset1:24
	ds_read2_b32 v[216:217], v21 offset0:49 offset1:57
	ds_read2_b32 v[218:219], v21 offset0:82 offset1:90
	ds_read2_b32 v[220:221], v21 offset0:115 offset1:123
	ds_read2_b32 v[222:223], v21 offset0:148 offset1:156
	ds_read2_b32 v[224:225], v21 offset0:181 offset1:189
	ds_read2_b32 v[226:227], v21 offset0:214 offset1:222
	ds_read2_b32 v[228:229], v21 offset0:247 offset1:255
	s_waitcnt lgkmcnt(0)
	v_max_f32_e32 v214, v214, v214
	v_max_f32_e32 v216, v216, v216
	v_max_f32_e32 v218, v218, v218
	v_max_f32_e32 v220, v220, v220
	v_max_f32_e32 v222, v222, v222
	v_max_f32_e32 v224, v224, v224
	v_max_f32_e32 v226, v226, v226
	v_max_f32_e32 v228, v228, v228
	v_med3_f32 v214, v214, s44, v64
	v_med3_f32 v216, v216, s44, v64
	v_med3_f32 v218, v218, s44, v64
	v_med3_f32 v220, v220, s44, v64
	v_med3_f32 v222, v222, s44, v64
	v_med3_f32 v224, v224, s44, v64
	v_med3_f32 v226, v226, s44, v64
	v_med3_f32 v228, v228, s44, v64
	v_mov_b32_e32 v230, v11
	v_mov_b32_e32 v231, v11
	v_or_b32_e32 v233, s36, v23
	v_cvt_pk_fp8_f32 v230, v214, v216
	v_cvt_pk_fp8_f32 v231, v222, v224
	v_lshl_add_u32 v232, v233, 14, v8
	v_cvt_pk_fp8_f32 v230, v218, v220 op_sel:[0,0,1]
	v_cvt_pk_fp8_f32 v231, v226, v228 op_sel:[0,0,1]
	s_nop 0
	global_store_dwordx2 v232, v[230:231], s[20:21]
	s_nop 1
	v_max_f32_e32 v215, v215, v215
	v_max_f32_e32 v217, v217, v217
	v_max_f32_e32 v219, v219, v219
	v_max_f32_e32 v221, v221, v221
	v_max_f32_e32 v223, v223, v223
	v_max_f32_e32 v225, v225, v225
	v_max_f32_e32 v227, v227, v227
	v_max_f32_e32 v229, v229, v229
	v_med3_f32 v215, v215, s44, v64
	v_med3_f32 v217, v217, s44, v64
	v_med3_f32 v219, v219, s44, v64
	v_med3_f32 v221, v221, s44, v64
	v_med3_f32 v223, v223, s44, v64
	v_med3_f32 v225, v225, s44, v64
	v_med3_f32 v227, v227, s44, v64
	v_med3_f32 v229, v229, s44, v64
	v_mov_b32_e32 v230, v11
	v_mov_b32_e32 v231, v11
	v_or_b32_e32 v233, s36, v24
	v_cvt_pk_fp8_f32 v230, v215, v217
	v_cvt_pk_fp8_f32 v231, v223, v225
	v_lshl_add_u32 v232, v233, 14, v8
	v_cvt_pk_fp8_f32 v230, v219, v221 op_sel:[0,0,1]
	v_cvt_pk_fp8_f32 v231, v227, v229 op_sel:[0,0,1]
	s_nop 0
	global_store_dwordx2 v232, v[230:231], s[20:21]
	s_nop 1
	s_waitcnt lgkmcnt(0)
	s_add_i32 s50, s50, s96
	s_add_i32 s39, s39, s76
	s_add_i32 s40, s40, s41
	s_add_i32 s42, s42, s43
	s_add_i32 s51, s51, s96
	s_branch .Lwd_orig
; #define GAS __attribute__((address_space(1)))
; #define LAS __attribute__((address_space(3)))
;     const int pr = item >> 1, kb = 2 * (pr / nblk) + (item & 1), nb = pr % nblk, k0 = 64 * kb, n0 = 32 * nb;
;     const int nr = n0 + (lane & 31); const int sc = MAP == 1 ? src_col_in(nr) : nr;
;     float v[32];
; #pragma unroll
;     for (int i = 0; i < 32; ++i) v[i] = sc >= 0 ? W[(size_t)(k0 + 2 * i + (lane >> 5)) * Nsrc + sc] : 0.f;
; #pragma unroll
;     for (int i = 0; i < 32; ++i) { const int k = k0 + 2 * i + (lane >> 5); float x = v[i] * wscale; if (KS) x *= (k < ksplit ? ksA[k] : ksB[k - ksplit]); scr[(2 * i + (lane >> 5)) * 33 + (lane & 31)] = x; }
;     LDS_WAIT(); asm volatile("" ::: "memory");
;     const int c = lane & 7;
; #pragma unroll
;     for (int j = 0; j < 4; ++j) { const int n = (lane >> 3) + 8 * j; const LAS float* s = scr + (8 * c) * 33 + n;
;         const unsigned long long o = (unsigned long long)pg8::pk4_fp8(s[0 * 33], s[1 * 33], s[2 * 33], s[3 * 33]) | ((unsigned long long)pg8::pk4_fp8(s[4 * 33], s[5 * 33], s[6 * 33], s[7 * 33]) << 32);
;         *(GAS unsigned long long*)(WT + (size_t)(n0 + n) * K + k0 + 8 * c) = o; }
;     LDS_WAIT(); asm volatile("" ::: "memory");
; }
; __global__ void __launch_bounds__(NWAVES * 64, 2) hybrid_fwd(Args args) {
;     ...
;         for (int it = gw; it < DEPTH * I_L; it += NGW) {
;             const int l = it / I_L; int r = it % I_L;
;             if (r < I_IN) { if (l >= PROJ_F8_FROM) p0_transpose_item_f8<true, 1>(args.in[2] + (size_t)l * DM * NSRC, DM, NSRC, NPROJ / 32, (unsigned char*)(ws + WS_WIN + l * SZ_WIN), WUP8_SCALE, args.in[1] + l * DM, args.in[1] + l * DM, DM, scr, r, lane);
;                 else p0_transpose_item<1, true>(args.in[2] + (size_t)l * DM * NSRC, DM, NSRC, NPROJ / 32, (bf16*)(ws + WS_WIN + l * SZ_WIN), args.in[1] + l * DM, args.in[1] + l * DM, DM, scr, r, lane); continue; } r -= I_IN;
;             if (r < I_O) { if (l >= WO_F8_FROM) p0_transpose_item_f8<true>(args.in[13] + (size_t)l * DM * DM, DM, DM, DM / 32, (unsigned char*)(ws + WS_WO + l * SZ_WO), 64.f, args.in[6] + l * 2048, args.in[12] + l * 2048, 2048, scr, r, lane);
;                 else p0_transpose_item<0, true>(args.in[13] + (size_t)l * DM * DM, DM, DM, DM / 32, (bf16*)(ws + WS_WO + l * SZ_WO), args.in[6] + l * 2048, args.in[12] + l * 2048, 2048, scr, r, lane); continue; } r -= I_O;
.Lwd_loopX_more:
	s_add_i32 s50, s50, s96
	s_add_i32 s39, s39, s76
	s_add_i32 s40, s40, s41
	s_add_i32 s42, s42, s43
	s_add_i32 s51, s51, s96
	s_add_i32 s20, s51, 0xffff0600
	s_lshr_b32 s4, s20, 7
	s_and_b32 s4, s4, 0xfe
	s_and_b32 s5, s20, 1
	s_or_b32 s4, s4, s5
	s_lshl_b32 s4, s4, 6
	s_lshl_b32 s5, s20, 4
	s_and_b32 s5, s5, 0xfe0
	s_waitcnt vmcnt(31)
	v_or_b32_e32 v208, s4, v6
	v_lshlrev_b32_e32 v208, 12, v208
	v_or3_b32 v208, s5, v18, v208
	v_lshlrev_b32_e32 v208, 2, v208
	s_mov_b64 s[8:9], s[10:11]
	global_load_dword v176, v208, s[8:9]
	s_add_u32 s8, s8, 0x8000
	s_addc_u32 s9, s9, 0
	global_load_dword v177, v208, s[8:9]
	s_add_u32 s8, s8, 0x8000
	s_addc_u32 s9, s9, 0
	global_load_dword v178, v208, s[8:9]
	s_add_u32 s8, s8, 0x8000
	s_addc_u32 s9, s9, 0
	global_load_dword v179, v208, s[8:9]
	s_add_u32 s8, s8, 0x8000
	s_addc_u32 s9, s9, 0
	global_load_dword v180, v208, s[8:9]
	s_add_u32 s8, s8, 0x8000
	s_addc_u32 s9, s9, 0
	global_load_dword v181, v208, s[8:9]
	s_add_u32 s8, s8, 0x8000
	s_addc_u32 s9, s9, 0
	global_load_dword v182, v208, s[8:9]
	s_add_u32 s8, s8, 0x8000
	s_addc_u32 s9, s9, 0
	global_load_dword v183, v208, s[8:9]
	s_add_u32 s8, s8, 0x8000
	s_addc_u32 s9, s9, 0
	global_load_dword v184, v208, s[8:9]
	s_add_u32 s8, s8, 0x8000
	s_addc_u32 s9, s9, 0
	global_load_dword v185, v208, s[8:9]
	s_add_u32 s8, s8, 0x8000
	s_addc_u32 s9, s9, 0
	global_load_dword v186, v208, s[8:9]
	s_add_u32 s8, s8, 0x8000
	s_addc_u32 s9, s9, 0
	global_load_dword v187, v208, s[8:9]
	s_add_u32 s8, s8, 0x8000
	s_addc_u32 s9, s9, 0
	global_load_dword v188, v208, s[8:9]
	s_add_u32 s8, s8, 0x8000
	s_addc_u32 s9, s9, 0
	global_load_dword v189, v208, s[8:9]
	s_add_u32 s8, s8, 0x8000
	s_addc_u32 s9, s9, 0
	global_load_dword v190, v208, s[8:9]
	s_add_u32 s8, s8, 0x8000
	s_addc_u32 s9, s9, 0
	global_load_dword v191, v208, s[8:9]
	s_add_u32 s8, s8, 0x8000
	s_addc_u32 s9, s9, 0
	global_load_dword v192, v208, s[8:9]
	s_add_u32 s8, s8, 0x8000
	s_addc_u32 s9, s9, 0
	global_load_dword v193, v208, s[8:9]
	s_add_u32 s8, s8, 0x8000
	s_addc_u32 s9, s9, 0
	global_load_dword v194, v208, s[8:9]
	s_add_u32 s8, s8, 0x8000
	s_addc_u32 s9, s9, 0
	global_load_dword v195, v208, s[8:9]
	s_add_u32 s8, s8, 0x8000
	s_addc_u32 s9, s9, 0
	global_load_dword v196, v208, s[8:9]
	s_add_u32 s8, s8, 0x8000
	s_addc_u32 s9, s9, 0
	global_load_dword v197, v208, s[8:9]
	s_add_u32 s8, s8, 0x8000
	s_addc_u32 s9, s9, 0
	global_load_dword v198, v208, s[8:9]
	s_add_u32 s8, s8, 0x8000
	s_addc_u32 s9, s9, 0
	global_load_dword v199, v208, s[8:9]
	s_add_u32 s8, s8, 0x8000
	s_addc_u32 s9, s9, 0
	global_load_dword v200, v208, s[8:9]
	s_add_u32 s8, s8, 0x8000
	s_addc_u32 s9, s9, 0
	global_load_dword v201, v208, s[8:9]
	s_add_u32 s8, s8, 0x8000
	s_addc_u32 s9, s9, 0
	global_load_dword v202, v208, s[8:9]
	s_add_u32 s8, s8, 0x8000
	s_addc_u32 s9, s9, 0
	global_load_dword v203, v208, s[8:9]
	s_add_u32 s8, s8, 0x8000
	s_addc_u32 s9, s9, 0
	global_load_dword v204, v208, s[8:9]
	s_add_u32 s8, s8, 0x8000
	s_addc_u32 s9, s9, 0
	global_load_dword v205, v208, s[8:9]
	s_add_u32 s8, s8, 0x8000
	s_addc_u32 s9, s9, 0
	global_load_dword v206, v208, s[8:9]
	s_add_u32 s8, s8, 0x8000
	s_addc_u32 s9, s9, 0
	global_load_dword v207, v208, s[8:9]
	s_waitcnt vmcnt(36)
	s_add_u32 s20, s30, s16
	s_addc_u32 s21, s31, 0
	v_add_u32_e32 v209, 0x1000, v19
	v_add_u32_e32 v210, 0x1400, v19
	v_add_u32_e32 v211, 0x1800, v19
	v_add_u32_e32 v212, 0x1c00, v19
	v_mul_f32_e32 v144, 0x43000000, v144
	v_mul_f32_e32 v145, 0x43000000, v145
	ds_write2_b32 v19, v144, v145 offset1:66
	v_mul_f32_e32 v146, 0x43000000, v146
	v_mul_f32_e32 v147, 0x43000000, v147
	ds_write2_b32 v19, v146, v147 offset0:132 offset1:198
	v_mul_f32_e32 v148, 0x43000000, v148
	v_mul_f32_e32 v149, 0x43000000, v149
	ds_write2_b32 v61, v148, v149 offset0:8 offset1:74
	v_mul_f32_e32 v150, 0x43000000, v150
	v_mul_f32_e32 v151, 0x43000000, v151
	ds_write2_b32 v61, v150, v151 offset0:140 offset1:206
	v_mul_f32_e32 v152, 0x43000000, v152
	v_mul_f32_e32 v153, 0x43000000, v153
	ds_write2_b32 v62, v152, v153 offset0:16 offset1:82
	v_mul_f32_e32 v154, 0x43000000, v154
	v_mul_f32_e32 v155, 0x43000000, v155
	ds_write2_b32 v62, v154, v155 offset0:148 offset1:214
	v_mul_f32_e32 v156, 0x43000000, v156
	v_mul_f32_e32 v157, 0x43000000, v157
	ds_write2_b32 v63, v156, v157 offset0:24 offset1:90
	v_mul_f32_e32 v158, 0x43000000, v158
	v_mul_f32_e32 v159, 0x43000000, v159
	ds_write2_b32 v63, v158, v159 offset0:156 offset1:222
	v_mul_f32_e32 v160, 0x43000000, v160
	v_mul_f32_e32 v161, 0x43000000, v161
	ds_write2_b32 v209, v160, v161 offset0:32 offset1:98
	v_mul_f32_e32 v162, 0x43000000, v162
	v_mul_f32_e32 v163, 0x43000000, v163
	ds_write2_b32 v209, v162, v163 offset0:164 offset1:230
	v_mul_f32_e32 v164, 0x43000000, v164
	v_mul_f32_e32 v165, 0x43000000, v165
	ds_write2_b32 v210, v164, v165 offset0:40 offset1:106
	v_mul_f32_e32 v166, 0x43000000, v166
	v_mul_f32_e32 v167, 0x43000000, v167
	ds_write2_b32 v210, v166, v167 offset0:172 offset1:238
	v_mul_f32_e32 v168, 0x43000000, v168
	v_mul_f32_e32 v169, 0x43000000, v169
	ds_write2_b32 v211, v168, v169 offset0:48 offset1:114
	v_mul_f32_e32 v170, 0x43000000, v170
	v_mul_f32_e32 v171, 0x43000000, v171
	ds_write2_b32 v211, v170, v171 offset0:180 offset1:246
	v_mul_f32_e32 v172, 0x43000000, v172
	v_mul_f32_e32 v173, 0x43000000, v173
	ds_write2_b32 v212, v172, v173 offset0:56 offset1:122
	v_mul_f32_e32 v174, 0x43000000, v174
	v_mul_f32_e32 v175, 0x43000000, v175
	ds_write2_b32 v212, v174, v175 offset0:188 offset1:254
	s_waitcnt lgkmcnt(0)
; #define GAS __attribute__((address_space(1)))
; #define LAS __attribute__((address_space(3)))
; #define LDS_WAIT() asm volatile("s_waitcnt lgkmcnt(0)" ::: "memory")
;     const int pr = item >> 1, kb = 2 * (pr / nblk) + (item & 1), nb = pr % nblk, k0 = 64 * kb, n0 = 32 * nb;
;     const int nr = n0 + (lane & 31); const int sc = MAP == 1 ? src_col_in(nr) : nr;
;     float v[32];
; #pragma unroll
;     for (int i = 0; i < 32; ++i) v[i] = sc >= 0 ? W[(size_t)(k0 + 2 * i + (lane >> 5)) * Nsrc + sc] : 0.f;
; #pragma unroll
;     for (int i = 0; i < 32; ++i) { const int k = k0 + 2 * i + (lane >> 5); float x = v[i] * wscale; if (KS) x *= (k < ksplit ? ksA[k] : ksB[k - ksplit]); scr[(2 * i + (lane >> 5)) * 33 + (lane & 31)] = x; }
;     LDS_WAIT(); asm volatile("" ::: "memory");
;     const int c = lane & 7;
; #pragma unroll
;     for (int j = 0; j < 4; ++j) { const int n = (lane >> 3) + 8 * j; const LAS float* s = scr + (8 * c) * 33 + n;
;         const unsigned long long o = (unsigned long long)pg8::pk4_fp8(s[0 * 33], s[1 * 33], s[2 * 33], s[3 * 33]) | ((unsigned long long)pg8::pk4_fp8(s[4 * 33], s[5 * 33], s[6 * 33], s[7 * 33]) << 32);
;         *(GAS unsigned long long*)(WT + (size_t)(n0 + n) * K + k0 + 8 * c) = o; }
;     LDS_WAIT(); asm volatile("" ::: "memory");
; }
	ds_read2_b32 v[214:215], v21 offset1:8
	ds_read2_b32 v[216:217], v21 offset0:33 offset1:41
	ds_read2_b32 v[218:219], v21 offset0:66 offset1:74
	ds_read2_b32 v[220:221], v21 offset0:99 offset1:107
	ds_read2_b32 v[222:223], v21 offset0:132 offset1:140
	ds_read2_b32 v[224:225], v21 offset0:165 offset1:173
	ds_read2_b32 v[226:227], v21 offset0:198 offset1:206
	ds_read2_b32 v[228:229], v21 offset0:231 offset1:239
	s_waitcnt lgkmcnt(0)
	v_max_f32_e32 v214, v214, v214
	v_max_f32_e32 v216, v216, v216
	v_max_f32_e32 v218, v218, v218
	v_max_f32_e32 v220, v220, v220
	v_max_f32_e32 v222, v222, v222
	v_max_f32_e32 v224, v224, v224
	v_max_f32_e32 v226, v226, v226
	v_max_f32_e32 v228, v228, v228
	v_med3_f32 v214, v214, s44, v64
	v_med3_f32 v216, v216, s44, v64
	v_med3_f32 v218, v218, s44, v64
	v_med3_f32 v220, v220, s44, v64
	v_med3_f32 v222, v222, s44, v64
	v_med3_f32 v224, v224, s44, v64
	v_med3_f32 v226, v226, s44, v64
	v_med3_f32 v228, v228, s44, v64
	v_mov_b32_e32 v230, v11
	v_mov_b32_e32 v231, v11
	v_or_b32_e32 v233, s36, v20
	v_cvt_pk_fp8_f32 v230, v214, v216
	v_cvt_pk_fp8_f32 v231, v222, v224
	v_lshl_add_u32 v232, v233, 14, v8
	v_cvt_pk_fp8_f32 v230, v218, v220 op_sel:[0,0,1]
	v_cvt_pk_fp8_f32 v231, v226, v228 op_sel:[0,0,1]
	s_nop 0
	global_store_dwordx2 v232, v[230:231], s[20:21]
	s_nop 1
	v_max_f32_e32 v215, v215, v215
	v_max_f32_e32 v217, v217, v217
	v_max_f32_e32 v219, v219, v219
	v_max_f32_e32 v221, v221, v221
	v_max_f32_e32 v223, v223, v223
	v_max_f32_e32 v225, v225, v225
	v_max_f32_e32 v227, v227, v227
	v_max_f32_e32 v229, v229, v229
	v_med3_f32 v215, v215, s44, v64
	v_med3_f32 v217, v217, s44, v64
	v_med3_f32 v219, v219, s44, v64
	v_med3_f32 v221, v221, s44, v64
	v_med3_f32 v223, v223, s44, v64
	v_med3_f32 v225, v225, s44, v64
	v_med3_f32 v227, v227, s44, v64
	v_med3_f32 v229, v229, s44, v64
	v_mov_b32_e32 v230, v11
	v_mov_b32_e32 v231, v11
	v_or_b32_e32 v233, s36, v22
	v_cvt_pk_fp8_f32 v230, v215, v217
	v_cvt_pk_fp8_f32 v231, v223, v225
	v_lshl_add_u32 v232, v233, 14, v8
	v_cvt_pk_fp8_f32 v230, v219, v221 op_sel:[0,0,1]
	v_cvt_pk_fp8_f32 v231, v227, v229 op_sel:[0,0,1]
	s_nop 0
	global_store_dwordx2 v232, v[230:231], s[20:21]
	s_nop 1
	ds_read2_b32 v[214:215], v21 offset0:16 offset1:24
	ds_read2_b32 v[216:217], v21 offset0:49 offset1:57
	ds_read2_b32 v[218:219], v21 offset0:82 offset1:90
	ds_read2_b32 v[220:221], v21 offset0:115 offset1:123
	ds_read2_b32 v[222:223], v21 offset0:148 offset1:156
	ds_read2_b32 v[224:225], v21 offset0:181 offset1:189
	ds_read2_b32 v[226:227], v21 offset0:214 offset1:222
	ds_read2_b32 v[228:229], v21 offset0:247 offset1:255
	s_waitcnt lgkmcnt(0)
	v_max_f32_e32 v214, v214, v214
	v_max_f32_e32 v216, v216, v216
	v_max_f32_e32 v218, v218, v218
	v_max_f32_e32 v220, v220, v220
	v_max_f32_e32 v222, v222, v222
	v_max_f32_e32 v224, v224, v224
	v_max_f32_e32 v226, v226, v226
	v_max_f32_e32 v228, v228, v228
	v_med3_f32 v214, v214, s44, v64
	v_med3_f32 v216, v216, s44, v64
	v_med3_f32 v218, v218, s44, v64
	v_med3_f32 v220, v220, s44, v64
	v_med3_f32 v222, v222, s44, v64
	v_med3_f32 v224, v224, s44, v64
	v_med3_f32 v226, v226, s44, v64
	v_med3_f32 v228, v228, s44, v64
	v_mov_b32_e32 v230, v11
	v_mov_b32_e32 v231, v11
	v_or_b32_e32 v233, s36, v23
	v_cvt_pk_fp8_f32 v230, v214, v216
	v_cvt_pk_fp8_f32 v231, v222, v224
	v_lshl_add_u32 v232, v233, 14, v8
	v_cvt_pk_fp8_f32 v230, v218, v220 op_sel:[0,0,1]
	v_cvt_pk_fp8_f32 v231, v226, v228 op_sel:[0,0,1]
	s_nop 0
	global_store_dwordx2 v232, v[230:231], s[20:21]
	s_nop 1
	v_max_f32_e32 v215, v215, v215
	v_max_f32_e32 v217, v217, v217
	v_max_f32_e32 v219, v219, v219
	v_max_f32_e32 v221, v221, v221
	v_max_f32_e32 v223, v223, v223
	v_max_f32_e32 v225, v225, v225
	v_max_f32_e32 v227, v227, v227
	v_max_f32_e32 v229, v229, v229
	v_med3_f32 v215, v215, s44, v64
	v_med3_f32 v217, v217, s44, v64
	v_med3_f32 v219, v219, s44, v64
	v_med3_f32 v221, v221, s44, v64
	v_med3_f32 v223, v223, s44, v64
	v_med3_f32 v225, v225, s44, v64
	v_med3_f32 v227, v227, s44, v64
	v_med3_f32 v229, v229, s44, v64
	v_mov_b32_e32 v230, v11
	v_mov_b32_e32 v231, v11
	v_or_b32_e32 v233, s36, v24
	v_cvt_pk_fp8_f32 v230, v215, v217
	v_cvt_pk_fp8_f32 v231, v223, v225
	v_lshl_add_u32 v232, v233, 14, v8
	v_cvt_pk_fp8_f32 v230, v219, v221 op_sel:[0,0,1]
	v_cvt_pk_fp8_f32 v231, v227, v229 op_sel:[0,0,1]
	s_nop 0
	global_store_dwordx2 v232, v[230:231], s[20:21]
	s_nop 1
	s_waitcnt lgkmcnt(0)
	s_mov_b32 s16, s4
	s_mov_b32 s36, s5
	s_branch .Lwd_loopY
; #define GAS __attribute__((address_space(1)))
; #define LAS __attribute__((address_space(3)))
; #define LDS_WAIT() asm volatile("s_waitcnt lgkmcnt(0)" ::: "memory")
;     const int pr = item >> 1, kb = 2 * (pr / nblk) + (item & 1), nb = pr % nblk, k0 = 64 * kb, n0 = 32 * nb;
;     const int nr = n0 + (lane & 31); const int sc = MAP == 1 ? src_col_in(nr) : nr;
;     float v[32];
; #pragma unroll
;     for (int i = 0; i < 32; ++i) v[i] = sc >= 0 ? W[(size_t)(k0 + 2 * i + (lane >> 5)) * Nsrc + sc] : 0.f;
; #pragma unroll
;     for (int i = 0; i < 32; ++i) { const int k = k0 + 2 * i + (lane >> 5); float x = v[i] * wscale; if (KS) x *= (k < ksplit ? ksA[k] : ksB[k - ksplit]); scr[(2 * i + (lane >> 5)) * 33 + (lane & 31)] = x; }
;     LDS_WAIT(); asm volatile("" ::: "memory");
;     const int c = lane & 7;
; #pragma unroll
;     for (int j = 0; j < 4; ++j) { const int n = (lane >> 3) + 8 * j; const LAS float* s = scr + (8 * c) * 33 + n;
;         const unsigned long long o = (unsigned long long)pg8::pk4_fp8(s[0 * 33], s[1 * 33], s[2 * 33], s[3 * 33]) | ((unsigned long long)pg8::pk4_fp8(s[4 * 33], s[5 * 33], s[6 * 33], s[7 * 33]) << 32);
;         *(GAS unsigned long long*)(WT + (size_t)(n0 + n) * K + k0 + 8 * c) = o; }
;     LDS_WAIT(); asm volatile("" ::: "memory");
; }
.Lwd_orig:
	s_add_i32 s16, s51, 0xffff0600
	v_readlane_b32 s4, v253, 35
	v_readlane_b32 s5, v253, 36
	s_add_u32 s30, s4, s60
	s_addc_u32 s31, s5, s61
	s_add_u32 s20, s81, s0
	s_addc_u32 s21, s94, s1
	s_lshr_b32 s16, s16, 7
	s_and_b32 s16, s16, 0xfe
	s_and_b32 s36, s51, 1
	s_or_b32 s16, s16, s36
	s_lshl_b32 s36, s16, 6
	s_add_i32 s16, s42, 0xfff06000
	v_or_b32_e32 v2, s36, v6
	s_and_b32 s16, s16, 0xfe0
	v_lshlrev_b32_e32 v2, 12, v2
	v_or3_b32 v3, s16, v18, v2
	v_or3_b32 v4, s16, v26, v2
	v_or3_b32 v5, s16, v27, v2
	v_or3_b32 v10, s16, v28, v2
	v_or3_b32 v16, s16, v29, v2
	v_or3_b32 v17, s16, v30, v2
	v_or3_b32 v65, s16, v31, v2
	v_or3_b32 v66, s16, v32, v2
	v_lshlrev_b32_e32 v3, 2, v3
	v_lshlrev_b32_e32 v4, 2, v4
	v_lshlrev_b32_e32 v5, 2, v5
	v_lshlrev_b32_e32 v10, 2, v10
	v_lshlrev_b32_e32 v16, 2, v16
	v_lshlrev_b32_e32 v17, 2, v17
	v_lshlrev_b32_e32 v65, 2, v65
	v_lshlrev_b32_e32 v66, 2, v66
	global_load_dword v3, v3, s[30:31]
	s_nop 0
	global_load_dword v4, v4, s[30:31]
	s_nop 0
	global_load_dword v5, v5, s[30:31]
	s_nop 0
	global_load_dword v10, v10, s[30:31]
	s_nop 0
	global_load_dword v16, v16, s[30:31]
	s_nop 0
	global_load_dword v17, v17, s[30:31]
	s_nop 0
	global_load_dword v65, v65, s[30:31]
	s_nop 0
	global_load_dword v66, v66, s[30:31]
	v_or3_b32 v67, s16, v33, v2
	v_or3_b32 v68, s16, v34, v2
	v_or3_b32 v69, s16, v35, v2
	v_or3_b32 v70, s16, v36, v2
	v_or3_b32 v71, s16, v37, v2
	v_or3_b32 v72, s16, v38, v2
	v_or3_b32 v73, s16, v39, v2
	v_or3_b32 v74, s16, v40, v2
	v_lshlrev_b32_e32 v67, 2, v67
	v_lshlrev_b32_e32 v68, 2, v68
	v_lshlrev_b32_e32 v69, 2, v69
	v_lshlrev_b32_e32 v70, 2, v70
	v_lshlrev_b32_e32 v71, 2, v71
	v_lshlrev_b32_e32 v72, 2, v72
	v_lshlrev_b32_e32 v73, 2, v73
	v_lshlrev_b32_e32 v74, 2, v74
	global_load_dword v67, v67, s[30:31]
	s_nop 0
	global_load_dword v68, v68, s[30:31]
	s_nop 0
	global_load_dword v69, v69, s[30:31]
	s_nop 0
	global_load_dword v70, v70, s[30:31]
	s_nop 0
	global_load_dword v71, v71, s[30:31]
	s_nop 0
	global_load_dword v72, v72, s[30:31]
	s_nop 0
	global_load_dword v73, v73, s[30:31]
	s_nop 0
	global_load_dword v74, v74, s[30:31]
	v_or3_b32 v75, s16, v41, v2
	v_or3_b32 v76, s16, v42, v2
	v_or3_b32 v77, s16, v43, v2
	v_or3_b32 v78, s16, v44, v2
	v_or3_b32 v79, s16, v45, v2
	v_or3_b32 v80, s16, v46, v2
	v_or3_b32 v81, s16, v47, v2
	v_or3_b32 v82, s16, v48, v2
	v_lshlrev_b32_e32 v75, 2, v75
	v_lshlrev_b32_e32 v76, 2, v76
	v_lshlrev_b32_e32 v77, 2, v77
	v_lshlrev_b32_e32 v78, 2, v78
	v_lshlrev_b32_e32 v79, 2, v79
	v_lshlrev_b32_e32 v80, 2, v80
	v_lshlrev_b32_e32 v81, 2, v81
	v_lshlrev_b32_e32 v82, 2, v82
	v_or3_b32 v83, s16, v49, v2
	v_or3_b32 v84, s16, v50, v2
	global_load_dword v75, v75, s[30:31]
	s_nop 0
	global_load_dword v76, v76, s[30:31]
	s_nop 0
	global_load_dword v77, v77, s[30:31]
	s_nop 0
	global_load_dword v78, v78, s[30:31]
	s_nop 0
	global_load_dword v79, v79, s[30:31]
	s_nop 0
	global_load_dword v80, v80, s[30:31]
	s_nop 0
	global_load_dword v81, v81, s[30:31]
	s_nop 0
	global_load_dword v82, v82, s[30:31]
	v_lshlrev_b32_e32 v83, 2, v83
	v_lshlrev_b32_e32 v84, 2, v84
	global_load_dword v83, v83, s[30:31]
	s_nop 0
	global_load_dword v84, v84, s[30:31]
	v_or3_b32 v85, s16, v51, v2
	v_or3_b32 v86, s16, v52, v2
	v_or3_b32 v87, s16, v53, v2
	v_or3_b32 v88, s16, v54, v2
	v_lshlrev_b32_e32 v85, 2, v85
	v_lshlrev_b32_e32 v86, 2, v86
	v_lshlrev_b32_e32 v87, 2, v87
	v_lshlrev_b32_e32 v88, 2, v88
	v_or3_b32 v89, s16, v55, v2
	v_or3_b32 v2, s16, v56, v2
	global_load_dword v85, v85, s[30:31]
	s_nop 0
	global_load_dword v86, v86, s[30:31]
	s_nop 0
	global_load_dword v87, v87, s[30:31]
	s_nop 0
	global_load_dword v88, v88, s[30:31]
	v_lshlrev_b32_e32 v89, 2, v89
	v_lshlrev_b32_e32 v2, 2, v2
	global_load_dword v89, v89, s[30:31]
	s_nop 0
	global_load_dword v2, v2, s[30:31]
	s_add_u32 s20, s20, s36
	s_addc_u32 s21, s21, 0
	v_readlane_b32 s6, v253, 37
	v_readlane_b32 s7, v253, 38
	v_readlane_b32 s8, v253, 39
	v_readlane_b32 s9, v253, 40
	v_readlane_b32 s10, v253, 41
	v_readlane_b32 s11, v253, 42
	s_waitcnt vmcnt(31)
	v_mul_f32_e32 v3, 0x43000000, v3
	s_waitcnt vmcnt(30)
	v_mul_f32_e32 v4, 0x43000000, v4
	ds_write2_b32 v19, v3, v4 offset1:66
	s_waitcnt vmcnt(29)
	v_mul_f32_e32 v3, 0x43000000, v5
	s_waitcnt vmcnt(28)
	v_mul_f32_e32 v4, 0x43000000, v10
	ds_write2_b32 v19, v3, v4 offset0:132 offset1:198
	s_waitcnt vmcnt(27)
	v_mul_f32_e32 v3, 0x43000000, v16
	s_waitcnt vmcnt(26)
	v_mul_f32_e32 v4, 0x43000000, v17
	ds_write2_b32 v61, v3, v4 offset0:8 offset1:74
	s_waitcnt vmcnt(25)
	v_mul_f32_e32 v3, 0x43000000, v65
	s_waitcnt vmcnt(24)
	v_mul_f32_e32 v4, 0x43000000, v66
	ds_write2_b32 v61, v3, v4 offset0:140 offset1:206
	v_add_u32_e32 v5, 0x1000, v19
	s_waitcnt vmcnt(23)
	v_mul_f32_e32 v3, 0x43000000, v67
	s_waitcnt vmcnt(22)
	v_mul_f32_e32 v4, 0x43000000, v68
	ds_write2_b32 v62, v3, v4 offset0:16 offset1:82
	s_waitcnt vmcnt(21)
	v_mul_f32_e32 v3, 0x43000000, v69
	s_waitcnt vmcnt(20)
	v_mul_f32_e32 v4, 0x43000000, v70
	ds_write2_b32 v62, v3, v4 offset0:148 offset1:214
	s_waitcnt vmcnt(19)
	v_mul_f32_e32 v3, 0x43000000, v71
	s_waitcnt vmcnt(18)
	v_mul_f32_e32 v4, 0x43000000, v72
	ds_write2_b32 v63, v3, v4 offset0:24 offset1:90
	s_waitcnt vmcnt(17)
	v_mul_f32_e32 v3, 0x43000000, v73
	s_waitcnt vmcnt(16)
	v_mul_f32_e32 v4, 0x43000000, v74
	ds_write2_b32 v63, v3, v4 offset0:156 offset1:222
	v_mov_b32_e32 v70, v11
	v_mov_b32_e32 v71, v11
	s_waitcnt vmcnt(15)
	v_mul_f32_e32 v3, 0x43000000, v75
	s_waitcnt vmcnt(14)
	v_mul_f32_e32 v4, 0x43000000, v76
	ds_write2_b32 v5, v3, v4 offset0:32 offset1:98
	s_waitcnt vmcnt(13)
	v_mul_f32_e32 v3, 0x43000000, v77
	s_waitcnt vmcnt(12)
; #define GAS __attribute__((address_space(1)))
; #define LAS __attribute__((address_space(3)))
; #define LDS_WAIT() asm volatile("s_waitcnt lgkmcnt(0)" ::: "memory")
;     const int pr = item >> 1, kb = 2 * (pr / nblk) + (item & 1), nb = pr % nblk, k0 = 64 * kb, n0 = 32 * nb;
;     const int nr = n0 + (lane & 31); const int sc = MAP == 1 ? src_col_in(nr) : nr;
;     float v[32];
; #pragma unroll
;     for (int i = 0; i < 32; ++i) v[i] = sc >= 0 ? W[(size_t)(k0 + 2 * i + (lane >> 5)) * Nsrc + sc] : 0.f;
; #pragma unroll
;     for (int i = 0; i < 32; ++i) { const int k = k0 + 2 * i + (lane >> 5); float x = v[i] * wscale; if (KS) x *= (k < ksplit ? ksA[k] : ksB[k - ksplit]); scr[(2 * i + (lane >> 5)) * 33 + (lane & 31)] = x; }
;     LDS_WAIT(); asm volatile("" ::: "memory");
;     const int c = lane & 7;
; #pragma unroll
;     for (int j = 0; j < 4; ++j) { const int n = (lane >> 3) + 8 * j; const LAS float* s = scr + (8 * c) * 33 + n;
;         const unsigned long long o = (unsigned long long)pg8::pk4_fp8(s[0 * 33], s[1 * 33], s[2 * 33], s[3 * 33]) | ((unsigned long long)pg8::pk4_fp8(s[4 * 33], s[5 * 33], s[6 * 33], s[7 * 33]) << 32);
;         *(GAS unsigned long long*)(WT + (size_t)(n0 + n) * K + k0 + 8 * c) = o; }
;     LDS_WAIT(); asm volatile("" ::: "memory");
; }
	v_mul_f32_e32 v4, 0x43000000, v78
	ds_write2_b32 v5, v3, v4 offset0:164 offset1:230
	s_waitcnt vmcnt(11)
	v_mul_f32_e32 v3, 0x43000000, v79
	s_waitcnt vmcnt(10)
	v_mul_f32_e32 v4, 0x43000000, v80
	v_add_u32_e32 v5, 0x1400, v19
	ds_write2_b32 v5, v3, v4 offset0:40 offset1:106
	s_waitcnt vmcnt(9)
	v_mul_f32_e32 v3, 0x43000000, v81
	s_waitcnt vmcnt(8)
	v_mul_f32_e32 v4, 0x43000000, v82
	ds_write2_b32 v5, v3, v4 offset0:172 offset1:238
	s_waitcnt vmcnt(7)
	v_mul_f32_e32 v3, 0x43000000, v83
	s_waitcnt vmcnt(6)
	v_mul_f32_e32 v4, 0x43000000, v84
	v_add_u32_e32 v5, 0x1800, v19
	ds_write2_b32 v5, v3, v4 offset0:48 offset1:114
	s_waitcnt vmcnt(5)
	v_mul_f32_e32 v3, 0x43000000, v85
	s_waitcnt vmcnt(4)
	v_mul_f32_e32 v4, 0x43000000, v86
	ds_write2_b32 v5, v3, v4 offset0:180 offset1:246
	s_waitcnt vmcnt(3)
	v_mul_f32_e32 v3, 0x43000000, v87
	s_waitcnt vmcnt(2)
	v_mul_f32_e32 v4, 0x43000000, v88
	v_add_u32_e32 v5, 0x1c00, v19
	ds_write2_b32 v5, v3, v4 offset0:56 offset1:122
	s_waitcnt vmcnt(1)
	v_mul_f32_e32 v3, 0x43000000, v89
	s_waitcnt vmcnt(0)
	v_mul_f32_e32 v2, 0x43000000, v2
	ds_write2_b32 v5, v3, v2 offset0:188 offset1:254
	s_waitcnt lgkmcnt(0)
	ds_read2_b32 v[2:3], v21 offset1:8
	ds_read2_b32 v[16:17], v21 offset0:33 offset1:41
	ds_read2_b32 v[66:67], v21 offset0:66 offset1:74
	ds_read2_b32 v[68:69], v21 offset0:99 offset1:107
	ds_read2_b32 v[72:73], v21 offset0:132 offset1:140
	ds_read2_b32 v[74:75], v21 offset0:165 offset1:173
	ds_read2_b32 v[76:77], v21 offset0:198 offset1:206
	ds_read2_b32 v[78:79], v21 offset0:231 offset1:239
	s_waitcnt lgkmcnt(6)
	v_max_f32_e32 v10, v16, v16
	v_max_f32_e32 v2, v2, v2
	v_med3_f32 v2, v2, s44, v64
	v_med3_f32 v10, v10, s44, v64
	v_cvt_pk_fp8_f32 v70, v2, v10
	s_waitcnt lgkmcnt(5)
	v_max_f32_e32 v16, v66, v66
	s_waitcnt lgkmcnt(4)
	v_max_f32_e32 v2, v68, v68
	v_med3_f32 v16, v16, s44, v64
	v_med3_f32 v2, v2, s44, v64
	v_cvt_pk_fp8_f32 v70, v16, v2 op_sel:[0,0,1]
	s_waitcnt lgkmcnt(3)
	v_max_f32_e32 v2, v72, v72
	s_waitcnt lgkmcnt(2)
	v_max_f32_e32 v10, v74, v74
	v_med3_f32 v2, v2, s44, v64
	v_med3_f32 v10, v10, s44, v64
	v_cvt_pk_fp8_f32 v71, v2, v10
	s_waitcnt lgkmcnt(1)
	v_max_f32_e32 v16, v76, v76
	s_waitcnt lgkmcnt(0)
	v_max_f32_e32 v10, v78, v78
	v_med3_f32 v2, v16, s44, v64
	v_med3_f32 v10, v10, s44, v64
	v_cvt_pk_fp8_f32 v71, v2, v10 op_sel:[0,0,1]
	v_or_b32_e32 v2, s16, v20
	v_lshlrev_b32_e32 v10, 14, v2
	v_max_f32_e32 v2, v3, v3
	v_lshl_add_u64 v[4:5], s[20:21], 0, v[8:9]
	v_med3_f32 v3, v2, s44, v64
	v_max_f32_e32 v2, v17, v17
	v_lshl_add_u64 v[80:81], v[4:5], 0, v[10:11]
	v_med3_f32 v10, v2, s44, v64
	v_mov_b32_e32 v2, v11
	v_cvt_pk_fp8_f32 v2, v3, v10
	v_max_f32_e32 v16, v67, v67
	v_max_f32_e32 v10, v69, v69
	v_med3_f32 v3, v16, s44, v64
	v_med3_f32 v10, v10, s44, v64
	v_cvt_pk_fp8_f32 v2, v3, v10 op_sel:[0,0,1]
	v_max_f32_e32 v3, v73, v73
	v_med3_f32 v10, v3, s44, v64
	v_max_f32_e32 v3, v75, v75
	v_med3_f32 v16, v3, s44, v64
	v_mov_b32_e32 v3, v11
	v_cvt_pk_fp8_f32 v3, v10, v16
	v_max_f32_e32 v17, v77, v77
	v_max_f32_e32 v16, v79, v79
	v_med3_f32 v10, v17, s44, v64
	v_med3_f32 v16, v16, s44, v64
	v_cvt_pk_fp8_f32 v3, v10, v16 op_sel:[0,0,1]
	v_or_b32_e32 v10, s16, v22
	v_lshlrev_b32_e32 v10, 14, v10
	v_lshl_add_u64 v[16:17], v[4:5], 0, v[10:11]
	ds_read2_b32 v[66:67], v21 offset0:16 offset1:24
	global_store_dwordx2 v[80:81], v[70:71], off
	global_store_dwordx2 v[16:17], v[2:3], off
	ds_read2_b32 v[2:3], v21 offset0:49 offset1:57
	ds_read2_b32 v[16:17], v21 offset0:82 offset1:90
	ds_read2_b32 v[68:69], v21 offset0:115 offset1:123
	v_mov_b32_e32 v70, v11
	s_waitcnt lgkmcnt(3)
	v_max_f32_e32 v10, v66, v66
	s_waitcnt lgkmcnt(2)
	v_max_f32_e32 v2, v2, v2
	v_med3_f32 v10, v10, s44, v64
	v_med3_f32 v2, v2, s44, v64
	ds_read2_b32 v[72:73], v21 offset0:148 offset1:156
	v_cvt_pk_fp8_f32 v70, v10, v2
	ds_read2_b32 v[74:75], v21 offset0:181 offset1:189
	ds_read2_b32 v[76:77], v21 offset0:214 offset1:222
	ds_read2_b32 v[78:79], v21 offset0:247 offset1:255
	s_waitcnt lgkmcnt(5)
	v_max_f32_e32 v16, v16, v16
	s_waitcnt lgkmcnt(4)
	v_max_f32_e32 v2, v68, v68
	v_med3_f32 v16, v16, s44, v64
	v_med3_f32 v2, v2, s44, v64
	v_cvt_pk_fp8_f32 v70, v16, v2 op_sel:[0,0,1]
	s_waitcnt lgkmcnt(3)
	v_max_f32_e32 v2, v72, v72
	s_waitcnt lgkmcnt(2)
	v_max_f32_e32 v10, v74, v74
	v_med3_f32 v2, v2, s44, v64
	v_med3_f32 v10, v10, s44, v64
	v_mov_b32_e32 v71, v11
	v_cvt_pk_fp8_f32 v71, v2, v10
	s_waitcnt lgkmcnt(1)
	v_max_f32_e32 v16, v76, v76
	s_waitcnt lgkmcnt(0)
	v_max_f32_e32 v10, v78, v78
	v_med3_f32 v2, v16, s44, v64
	v_med3_f32 v10, v10, s44, v64
	v_cvt_pk_fp8_f32 v71, v2, v10 op_sel:[0,0,1]
	v_or_b32_e32 v2, s16, v23
	v_lshlrev_b32_e32 v10, 14, v2
	v_max_f32_e32 v2, v67, v67
	v_lshl_add_u64 v[80:81], v[4:5], 0, v[10:11]
	v_med3_f32 v10, v2, s44, v64
	v_max_f32_e32 v2, v3, v3
	v_med3_f32 v3, v2, s44, v64
	v_mov_b32_e32 v2, v11
	v_cvt_pk_fp8_f32 v2, v10, v3
	v_max_f32_e32 v16, v17, v17
	v_max_f32_e32 v10, v69, v69
	v_med3_f32 v3, v16, s44, v64
	v_med3_f32 v10, v10, s44, v64
	v_cvt_pk_fp8_f32 v2, v3, v10 op_sel:[0,0,1]
	v_max_f32_e32 v3, v73, v73
	v_med3_f32 v10, v3, s44, v64
	v_max_f32_e32 v3, v75, v75
	v_med3_f32 v16, v3, s44, v64
	v_mov_b32_e32 v3, v11
	v_cvt_pk_fp8_f32 v3, v10, v16
	v_max_f32_e32 v17, v77, v77
	v_max_f32_e32 v16, v79, v79
	v_med3_f32 v10, v17, s44, v64
	v_med3_f32 v16, v16, s44, v64
	v_cvt_pk_fp8_f32 v3, v10, v16 op_sel:[0,0,1]
	v_or_b32_e32 v10, s16, v24
	v_lshlrev_b32_e32 v10, 14, v10
	v_lshl_add_u64 v[4:5], v[4:5], 0, v[10:11]
	global_store_dwordx2 v[80:81], v[70:71], off
	global_store_dwordx2 v[4:5], v[2:3], off
	s_waitcnt lgkmcnt(0)
	s_mov_b64 s[20:21], 0
